# v037 + dead fp8 zero-init movs in the MoE epilogues turned into s_nop + P13 mask word read hoisted behind the tile barrier
# speedup vs baseline: 1.0109x; 1.0104x over previous
.LBB0_511:
	s_lshl_b32 s1, s28, 2
	s_add_i32 s1, s1, 0
	s_add_i32 s1, s1, 0x20480
	v_mov_b32_e32 v42, s1
	ds_read_b32 v42, v42
	s_ashr_i32 s29, s28, 31
	v_lshl_or_b32 v169, s26, 7, v170
	s_lshl_b64 s[18:19], s[28:29], 13
	v_readlane_b32 s84, v252, 0
	s_waitcnt lgkmcnt(0)
	v_sub_u32_e32 v42, s56, v42
	v_lshl_add_u32 v184, v42, 8, v189
	v_readlane_b32 s85, v252, 1
	s_add_u32 s22, s84, s18
	v_lshlrev_b32_e32 v42, 1, v169
	s_addc_u32 s23, s85, s19
	v_ashrrev_i32_e32 v43, 31, v42
	v_lshl_add_u64 v[50:51], v[42:43], 2, s[22:23]
	global_load_dwordx4 v[42:45], v[50:51], off offset:48
	global_load_dwordx4 v[46:49], v[50:51], off offset:32
	global_load_dwordx4 v[66:69], v[50:51], off offset:16
	global_load_dwordx4 v[70:73], v[50:51], off
	s_add_u32 s1, s46, s18
	s_addc_u32 s21, s47, s19
	s_lshl_b32 s18, s26, 8
	s_ashr_i32 s19, s18, 31
	s_lshl_b64 s[18:19], s[18:19], 2
	s_add_u32 s18, s1, s18
	s_addc_u32 s19, s21, s19
	v_ashrrev_i32_e32 v185, 31, v184
	v_cvt_f32_i32_e32 v151, v151
	v_cvt_f32_i32_e32 v150, v150
	v_cvt_f32_i32_e32 v159, v159
	v_cvt_f32_i32_e32 v158, v158
	v_cvt_f32_i32_e32 v147, v147
	v_cvt_f32_i32_e32 v146, v146
	v_cvt_f32_i32_e32 v155, v155
	v_cvt_f32_i32_e32 v154, v154
	v_cvt_f32_i32_e32 v149, v149
	v_cvt_f32_i32_e32 v148, v148
	v_cvt_f32_i32_e32 v157, v157
	v_cvt_f32_i32_e32 v156, v156
	v_cvt_f32_i32_e32 v131, v131
	v_cvt_f32_i32_e32 v130, v130
	v_cvt_f32_i32_e32 v133, v133
	v_cvt_f32_i32_e32 v132, v132
	v_sub_u32_e32 v172, v169, v190
	v_ashrrev_i32_e32 v173, 31, v172
	v_cvt_f32_i32_e32 v115, v115
	v_cvt_f32_i32_e32 v114, v114
	v_cvt_f32_i32_e32 v117, v117
	v_cvt_f32_i32_e32 v116, v116
	v_cvt_f32_i32_e32 v99, v99
	v_cvt_f32_i32_e32 v98, v98
	v_cvt_f32_i32_e32 v101, v101
	v_cvt_f32_i32_e32 v100, v100
	v_cvt_f32_i32_e32 v83, v83
	v_cvt_f32_i32_e32 v82, v82
	v_cvt_f32_i32_e32 v85, v85
	v_cvt_f32_i32_e32 v84, v84
	v_cvt_f32_i32_e32 v59, v59
	v_cvt_f32_i32_e32 v58, v58
	v_cvt_f32_i32_e32 v61, v61
	v_cvt_f32_i32_e32 v60, v60
	v_cvt_f32_i32_e32 v39, v39
	v_cvt_f32_i32_e32 v38, v38
	v_cvt_f32_i32_e32 v23, v23
	v_cvt_f32_i32_e32 v22, v22
	v_cvt_f32_i32_e32 v25, v25
	v_cvt_f32_i32_e32 v24, v24
	v_cvt_f32_i32_e32 v19, v19
	v_cvt_f32_i32_e32 v18, v18
	v_cvt_f32_i32_e32 v11, v11
	v_cvt_f32_i32_e32 v10, v10
	v_cvt_f32_i32_e32 v15, v15
	v_cvt_f32_i32_e32 v14, v14
	v_cvt_f32_i32_e32 v13, v13
	v_cvt_f32_i32_e32 v12, v12
	v_cvt_f32_i32_e32 v3, v3
	v_cvt_f32_i32_e32 v2, v2
	v_cvt_f32_i32_e32 v7, v7
	v_cvt_f32_i32_e32 v6, v6
	v_cvt_f32_i32_e32 v5, v5
	v_cvt_f32_i32_e32 v4, v4
	v_readlane_b32 s86, v252, 2
	v_readlane_b32 s87, v252, 3
	v_readlane_b32 s88, v252, 4
	v_readlane_b32 s89, v252, 5
	v_readlane_b32 s90, v252, 6
	v_readlane_b32 s91, v252, 7
	s_waitcnt vmcnt(0)
	v_mov_b32_e32 v50, v67
	v_mov_b32_e32 v51, v69
	v_pk_add_f32 v[180:181], v[50:51], 1.0 op_sel_hi:[1,0]
	v_mov_b32_e32 v50, v71
	v_mov_b32_e32 v51, v73
	v_pk_add_f32 v[182:183], v[50:51], 1.0 op_sel_hi:[1,0]
	v_mov_b32_e32 v50, v43
	v_mov_b32_e32 v51, v45
	v_pk_add_f32 v[176:177], v[50:51], 1.0 op_sel_hi:[1,0]
	v_mov_b32_e32 v50, v47
	v_mov_b32_e32 v51, v49
	v_lshlrev_b32_e32 v43, 2, v170
	v_pk_add_f32 v[178:179], v[50:51], 1.0 op_sel_hi:[1,0]
	global_load_dwordx4 v[50:53], v43, s[18:19] offset:16
	global_load_dwordx4 v[74:77], v43, s[18:19]
	global_load_dwordx4 v[54:57], v43, s[18:19] offset:528
	global_load_dwordx4 v[78:81], v43, s[18:19] offset:512
	s_lshl_b64 s[18:19], s[28:29], 18
	s_add_u32 s18, s66, s18
	s_addc_u32 s19, s67, s19
	v_lshl_add_u64 v[184:185], v[184:185], 2, s[18:19]
	global_load_dword v212, v[184:185], off
	v_mov_b32_e32 v43, v44
	global_load_dword v44, v[184:185], off offset:64
	global_load_dword v220, v[184:185], off offset:128
	global_load_dword v222, v[184:185], off offset:192
	global_load_dword v224, v[184:185], off offset:512
	global_load_dword v226, v[184:185], off offset:576
	global_load_dword v228, v[184:185], off offset:640
	global_load_dword v230, v[184:185], off offset:704
	v_mov_b32_e32 v47, v48
	v_mov_b32_e32 v71, v72
	v_mov_b32_e32 v67, v68
	v_lshl_add_u32 v45, s56, 8, v189
	s_mov_b64 s[18:19], -1
	s_and_b64 vcc, exec, s[2:3]
	s_waitcnt vmcnt(11)
	v_pk_mul_f32 v[48:49], v[50:51], v[150:151]
	s_waitcnt vmcnt(10)
	v_pk_mul_f32 v[72:73], v[74:75], v[158:159]
	s_waitcnt vmcnt(9)
	v_pk_mul_f32 v[146:147], v[54:55], v[146:147]
	s_waitcnt vmcnt(8)
	v_pk_mul_f32 v[154:155], v[78:79], v[154:155]
	v_pk_mul_f32 v[148:149], v[56:57], v[148:149]
	v_pk_mul_f32 v[130:131], v[54:55], v[130:131]
	v_pk_mul_f32 v[132:133], v[56:57], v[132:133]
	v_pk_mul_f32 v[114:115], v[54:55], v[114:115]
	s_waitcnt vmcnt(7)
	v_pk_fma_f32 v[48:49], v[48:49], v[212:213], v[46:47] op_sel_hi:[1,0,1]
	v_pk_fma_f32 v[72:73], v[72:73], v[212:213], v[70:71] op_sel_hi:[1,0,1]
	v_min_f32_e32 v48, 0x40e00000, v48
	v_min_f32_e32 v49, 0x40e00000, v49
	v_pk_mul_f32 v[150:151], v[48:49], s[12:13] op_sel_hi:[1,0]
	v_pk_fma_f32 v[146:147], v[146:147], v[212:213], v[178:179] op_sel_hi:[1,0,1]
	v_exp_f32_e32 v150, v150
	v_exp_f32_e32 v151, v151
	v_min_f32_e32 v72, 0x40e00000, v72
	v_min_f32_e32 v73, 0x40e00000, v73
	v_med3_f32 v146, v146, s54, v210
	v_pk_fma_f32 v[150:151], v[150:151], s[14:15], s[14:15] op_sel_hi:[1,0,0]
	v_med3_f32 v147, v147, s54, v210
	v_rcp_f32_e32 v150, v150
	v_rcp_f32_e32 v151, v151
	v_pk_mul_f32 v[158:159], v[72:73], s[12:13] op_sel_hi:[1,0]
	v_pk_fma_f32 v[154:155], v[154:155], v[212:213], v[182:183] op_sel_hi:[1,0,1]
	v_exp_f32_e32 v158, v158
	v_pk_mul_f32 v[48:49], v[48:49], v[150:151]
	v_exp_f32_e32 v159, v159
	v_pk_mul_f32 v[48:49], v[146:147], v[48:49]
	v_cvt_f32_i32_e32 v147, v153
	v_cvt_f32_i32_e32 v146, v152
	v_pk_fma_f32 v[158:159], v[158:159], s[14:15], s[14:15] op_sel_hi:[1,0,0]
	v_med3_f32 v154, v154, s54, v210
	v_rcp_f32_e32 v158, v158
	v_pk_mul_f32 v[146:147], v[52:53], v[146:147]
	v_rcp_f32_e32 v159, v159
	v_pk_fma_f32 v[146:147], v[146:147], v[212:213], v[42:43] op_sel_hi:[1,0,1]
	v_med3_f32 v155, v155, s54, v210
	v_min_f32_e32 v146, 0x40e00000, v146
	v_min_f32_e32 v147, 0x40e00000, v147
	v_pk_mul_f32 v[150:151], v[146:147], s[12:13] op_sel_hi:[1,0]
	v_pk_mul_f32 v[72:73], v[72:73], v[158:159]
	v_exp_f32_e32 v150, v150
	v_exp_f32_e32 v151, v151
	v_pk_mul_f32 v[72:73], v[154:155], v[72:73]
	v_cvt_f32_i32_e32 v155, v161
	v_cvt_f32_i32_e32 v154, v160
	v_pk_fma_f32 v[150:151], v[150:151], s[14:15], s[14:15] op_sel_hi:[1,0,0]
	v_pk_fma_f32 v[148:149], v[148:149], v[212:213], v[176:177] op_sel_hi:[1,0,1]
	v_rcp_f32_e32 v150, v150
	v_rcp_f32_e32 v151, v151
	v_pk_mul_f32 v[68:69], v[76:77], v[154:155]
	v_med3_f32 v148, v148, s54, v210
	v_pk_fma_f32 v[68:69], v[68:69], v[212:213], v[66:67] op_sel_hi:[1,0,1]
	v_med3_f32 v149, v149, s54, v210
	v_min_f32_e32 v68, 0x40e00000, v68
	v_min_f32_e32 v69, 0x40e00000, v69
	v_pk_mul_f32 v[146:147], v[146:147], v[150:151]
	v_pk_mul_f32 v[154:155], v[80:81], v[156:157]
	v_pk_mul_f32 v[156:157], v[68:69], s[12:13] op_sel_hi:[1,0]
	v_pk_mul_f32 v[148:149], v[148:149], v[146:147]
	s_nop 0
	v_exp_f32_e32 v156, v156
	v_exp_f32_e32 v157, v157
	v_cvt_pk_fp8_f32 v147, v48, v49
	v_cvt_f32_i32_e32 v49, v143
	v_cvt_f32_i32_e32 v48, v142
	v_pk_fma_f32 v[156:157], v[156:157], s[14:15], s[14:15] op_sel_hi:[1,0,0]
	s_nop 0
	v_rcp_f32_e32 v156, v156
	v_pk_mul_f32 v[48:49], v[74:75], v[48:49]
	v_rcp_f32_e32 v157, v157
	s_waitcnt vmcnt(6)
	v_pk_fma_f32 v[48:49], v[48:49], v[44:45], v[70:71] op_sel_hi:[1,0,1]
	v_cvt_pk_fp8_f32 v146, v72, v73
	v_min_f32_e32 v48, 0x40e00000, v48
	v_min_f32_e32 v49, 0x40e00000, v49
	v_pk_mul_f32 v[72:73], v[48:49], s[12:13] op_sel_hi:[1,0]
	v_pk_fma_f32 v[154:155], v[154:155], v[212:213], v[180:181] op_sel_hi:[1,0,1]
	v_exp_f32_e32 v72, v72
	v_exp_f32_e32 v73, v73
	v_med3_f32 v154, v154, s54, v210
	v_med3_f32 v155, v155, s54, v210
	v_pk_mul_f32 v[68:69], v[68:69], v[156:157]
	v_pk_fma_f32 v[72:73], v[72:73], s[14:15], s[14:15] op_sel_hi:[1,0,0]
	v_pk_mul_f32 v[68:69], v[154:155], v[68:69]
	v_rcp_f32_e32 v72, v72
	v_cvt_pk_fp8_f32 v146, v68, v69 op_sel:[0,0,1]
	v_cvt_f32_i32_e32 v69, v139
	v_cvt_f32_i32_e32 v68, v138
	v_rcp_f32_e32 v73, v73
	v_pk_fma_f32 v[130:131], v[130:131], v[44:45], v[178:179] op_sel_hi:[1,0,1]
	v_cvt_pk_fp8_f32 v147, v148, v149 op_sel:[0,0,1]
	v_pk_mul_f32 v[68:69], v[78:79], v[68:69]
	v_pk_mul_f32 v[48:49], v[48:49], v[72:73]
	v_pk_fma_f32 v[68:69], v[68:69], v[44:45], v[182:183] op_sel_hi:[1,0,1]
	v_cvt_f32_i32_e32 v73, v141
	v_med3_f32 v68, v68, s54, v210
	v_med3_f32 v69, v69, s54, v210
	v_pk_mul_f32 v[48:49], v[68:69], v[48:49]
	v_cvt_f32_i32_e32 v69, v145
	v_cvt_f32_i32_e32 v68, v144
	v_cvt_f32_i32_e32 v72, v140
	v_med3_f32 v130, v130, s54, v210
	v_med3_f32 v131, v131, s54, v210
	v_pk_mul_f32 v[68:69], v[76:77], v[68:69]
	v_pk_mul_f32 v[72:73], v[80:81], v[72:73]
	v_pk_fma_f32 v[68:69], v[68:69], v[44:45], v[66:67] op_sel_hi:[1,0,1]
	v_pk_fma_f32 v[72:73], v[72:73], v[44:45], v[180:181] op_sel_hi:[1,0,1]
	v_min_f32_e32 v68, 0x40e00000, v68
	v_min_f32_e32 v69, 0x40e00000, v69
	v_pk_mul_f32 v[138:139], v[68:69], s[12:13] op_sel_hi:[1,0]
	v_med3_f32 v72, v72, s54, v210
	v_exp_f32_e32 v138, v138
	v_exp_f32_e32 v139, v139
	v_med3_f32 v73, v73, s54, v210
	s_nop 0
	s_nop 0
	v_pk_fma_f32 v[138:139], v[138:139], s[14:15], s[14:15] op_sel_hi:[1,0,0]
	v_cvt_pk_fp8_f32 v148, v48, v49
	v_rcp_f32_e32 v138, v138
	v_rcp_f32_e32 v139, v139
	v_pk_fma_f32 v[132:133], v[132:133], v[44:45], v[176:177] op_sel_hi:[1,0,1]
	v_or_b32_e32 v48, v45, v191
	v_med3_f32 v132, v132, s54, v210
	v_pk_mul_f32 v[68:69], v[68:69], v[138:139]
	v_med3_f32 v133, v133, s54, v210
	v_pk_mul_f32 v[68:69], v[72:73], v[68:69]
	v_cvt_f32_i32_e32 v73, v135
	v_cvt_f32_i32_e32 v72, v134
	v_cvt_pk_fp8_f32 v148, v68, v69 op_sel:[0,0,1]
	v_ashrrev_i32_e32 v49, 31, v48
	v_lshlrev_b64 v[48:49], 10, v[48:49]
	v_pk_mul_f32 v[72:73], v[50:51], v[72:73]
	v_lshl_add_u64 v[48:49], s[94:95], 0, v[48:49]
	v_pk_fma_f32 v[72:73], v[72:73], v[44:45], v[46:47] op_sel_hi:[1,0,1]
	v_permlane16_swap_b32_e32 v146, v148
	v_min_f32_e32 v72, 0x40e00000, v72
	v_min_f32_e32 v73, 0x40e00000, v73
	v_pk_mul_f32 v[134:135], v[72:73], s[12:13] op_sel_hi:[1,0]
	v_lshl_add_u64 v[48:49], v[48:49], 0, v[172:173]
	v_exp_f32_e32 v134, v134
	v_exp_f32_e32 v135, v135
	v_cvt_f32_i32_e32 v69, v123
	v_cvt_f32_i32_e32 v68, v122
	v_pk_mul_f32 v[116:117], v[56:57], v[116:117]
	v_pk_fma_f32 v[134:135], v[134:135], s[14:15], s[14:15] op_sel_hi:[1,0,0]
	v_pk_mul_f32 v[98:99], v[54:55], v[98:99]
	v_rcp_f32_e32 v134, v134
	v_rcp_f32_e32 v135, v135
	v_pk_mul_f32 v[68:69], v[78:79], v[68:69]
	v_pk_mul_f32 v[100:101], v[56:57], v[100:101]
	v_pk_mul_f32 v[82:83], v[54:55], v[82:83]
	v_pk_mul_f32 v[72:73], v[72:73], v[134:135]
	v_pk_mul_f32 v[84:85], v[56:57], v[84:85]
	v_pk_mul_f32 v[72:73], v[130:131], v[72:73]
	v_cvt_f32_i32_e32 v131, v137
	v_cvt_f32_i32_e32 v130, v136
	v_cvt_pk_fp8_f32 v149, v72, v73
	v_pk_mul_f32 v[58:59], v[78:79], v[58:59]
	v_pk_mul_f32 v[60:61], v[80:81], v[60:61]
	v_pk_mul_f32 v[130:131], v[52:53], v[130:131]
	v_pk_mul_f32 v[38:39], v[50:51], v[38:39]
	v_pk_fma_f32 v[130:131], v[130:131], v[44:45], v[42:43] op_sel_hi:[1,0,1]
	v_pk_mul_f32 v[22:23], v[54:55], v[22:23]
	v_min_f32_e32 v130, 0x40e00000, v130
	v_min_f32_e32 v131, 0x40e00000, v131
	v_pk_mul_f32 v[134:135], v[130:131], s[12:13] op_sel_hi:[1,0]
	v_pk_mul_f32 v[24:25], v[56:57], v[24:25]
	v_exp_f32_e32 v134, v134
	v_exp_f32_e32 v135, v135
	v_pk_mul_f32 v[18:19], v[50:51], v[18:19]
	v_pk_mul_f32 v[10:11], v[74:75], v[10:11]
	v_pk_mul_f32 v[14:15], v[78:79], v[14:15]
	v_pk_fma_f32 v[134:135], v[134:135], s[14:15], s[14:15] op_sel_hi:[1,0,0]
	v_pk_mul_f32 v[12:13], v[76:77], v[12:13]
	v_rcp_f32_e32 v134, v134
	v_rcp_f32_e32 v135, v135
	v_pk_mul_f32 v[2:3], v[50:51], v[2:3]
	v_pk_mul_f32 v[6:7], v[54:55], v[6:7]
	v_pk_mul_f32 v[4:5], v[52:53], v[4:5]
	v_pk_mul_f32 v[130:131], v[130:131], v[134:135]
	s_nop 0
	v_pk_mul_f32 v[130:131], v[132:133], v[130:131]
	s_nop 0
	v_cvt_pk_fp8_f32 v149, v130, v131 op_sel:[0,0,1]
	s_nop 1
	v_permlane16_swap_b32_e32 v147, v149
	global_store_dwordx4 v[48:49], v[146:149], off
	s_nop 0
	v_cvt_f32_i32_e32 v49, v127
	v_cvt_f32_i32_e32 v48, v126
	v_pk_mul_f32 v[48:49], v[74:75], v[48:49]
	s_waitcnt vmcnt(6)
	v_pk_fma_f32 v[48:49], v[48:49], v[220:221], v[70:71] op_sel_hi:[1,0,1]
	s_nop 0
	v_min_f32_e32 v48, 0x40e00000, v48
	v_min_f32_e32 v49, 0x40e00000, v49
	v_pk_mul_f32 v[72:73], v[48:49], s[12:13] op_sel_hi:[1,0]
	v_pk_fma_f32 v[68:69], v[68:69], v[220:221], v[182:183] op_sel_hi:[1,0,1]
	v_exp_f32_e32 v72, v72
	v_exp_f32_e32 v73, v73
	v_med3_f32 v68, v68, s54, v210
	v_med3_f32 v69, v69, s54, v210
	v_pk_fma_f32 v[114:115], v[114:115], v[220:221], v[178:179] op_sel_hi:[1,0,1]
	v_pk_fma_f32 v[72:73], v[72:73], s[14:15], s[14:15] op_sel_hi:[1,0,0]
	v_med3_f32 v114, v114, s54, v210
	v_rcp_f32_e32 v72, v72
	v_rcp_f32_e32 v73, v73
	v_med3_f32 v115, v115, s54, v210
	v_pk_fma_f32 v[116:117], v[116:117], v[220:221], v[176:177] op_sel_hi:[1,0,1]
	v_pk_mul_f32 v[48:49], v[48:49], v[72:73]
	s_nop 0
	v_pk_mul_f32 v[48:49], v[68:69], v[48:49]
	v_cvt_f32_i32_e32 v69, v129
	v_cvt_f32_i32_e32 v68, v128
	v_cvt_f32_i32_e32 v73, v125
	v_cvt_f32_i32_e32 v72, v124
	v_med3_f32 v116, v116, s54, v210
	v_pk_mul_f32 v[68:69], v[76:77], v[68:69]
	v_med3_f32 v117, v117, s54, v210
	v_pk_fma_f32 v[68:69], v[68:69], v[220:221], v[66:67] op_sel_hi:[1,0,1]
	v_pk_mul_f32 v[72:73], v[80:81], v[72:73]
	v_min_f32_e32 v68, 0x40e00000, v68
	v_min_f32_e32 v69, 0x40e00000, v69
	v_pk_mul_f32 v[122:123], v[68:69], s[12:13] op_sel_hi:[1,0]
	v_pk_fma_f32 v[72:73], v[72:73], v[220:221], v[180:181] op_sel_hi:[1,0,1]
	v_exp_f32_e32 v122, v122
	v_exp_f32_e32 v123, v123
	v_med3_f32 v72, v72, s54, v210
	v_med3_f32 v73, v73, s54, v210
	v_pk_fma_f32 v[122:123], v[122:123], s[14:15], s[14:15] op_sel_hi:[1,0,0]
	s_nop 0
	v_rcp_f32_e32 v122, v122
	v_rcp_f32_e32 v123, v123
	s_nop 0
	v_pk_mul_f32 v[68:69], v[68:69], v[122:123]
	s_nop 0
	v_pk_mul_f32 v[68:69], v[72:73], v[68:69]
	v_cvt_f32_i32_e32 v73, v119
	v_cvt_f32_i32_e32 v72, v118
	v_pk_mul_f32 v[72:73], v[50:51], v[72:73]
	s_nop 0
	v_pk_fma_f32 v[72:73], v[72:73], v[220:221], v[46:47] op_sel_hi:[1,0,1]
	s_nop 0
	v_min_f32_e32 v72, 0x40e00000, v72
	v_min_f32_e32 v73, 0x40e00000, v73
	v_pk_mul_f32 v[118:119], v[72:73], s[12:13] op_sel_hi:[1,0]
	s_nop 0
	v_exp_f32_e32 v118, v118
	v_exp_f32_e32 v119, v119
	s_nop 0
	v_pk_fma_f32 v[118:119], v[118:119], s[14:15], s[14:15] op_sel_hi:[1,0,0]
	s_nop 0
	v_rcp_f32_e32 v118, v118
	v_rcp_f32_e32 v119, v119
	s_nop 0
	v_pk_mul_f32 v[72:73], v[72:73], v[118:119]
	s_nop 0
	v_pk_mul_f32 v[72:73], v[114:115], v[72:73]
	v_cvt_f32_i32_e32 v115, v121
	v_cvt_f32_i32_e32 v114, v120
	v_pk_mul_f32 v[114:115], v[52:53], v[114:115]
	s_nop 0
	v_pk_fma_f32 v[114:115], v[114:115], v[220:221], v[42:43] op_sel_hi:[1,0,1]
	s_nop 0
	v_min_f32_e32 v114, 0x40e00000, v114
	v_min_f32_e32 v115, 0x40e00000, v115
	v_pk_mul_f32 v[118:119], v[114:115], s[12:13] op_sel_hi:[1,0]
	s_waitcnt vmcnt(5)
	v_pk_fma_f32 v[98:99], v[98:99], v[222:223], v[178:179] op_sel_hi:[1,0,1]
	v_exp_f32_e32 v118, v118
	v_exp_f32_e32 v119, v119
	v_med3_f32 v98, v98, s54, v210
	v_med3_f32 v99, v99, s54, v210
	v_pk_fma_f32 v[100:101], v[100:101], v[222:223], v[176:177] op_sel_hi:[1,0,1]
	v_pk_fma_f32 v[118:119], v[118:119], s[14:15], s[14:15] op_sel_hi:[1,0,0]
	v_med3_f32 v100, v100, s54, v210
	v_rcp_f32_e32 v118, v118
	v_rcp_f32_e32 v119, v119
	v_med3_f32 v101, v101, s54, v210
	v_pk_mul_f32 v[114:115], v[114:115], v[118:119]
	s_nop 0
	v_pk_mul_f32 v[116:117], v[116:117], v[114:115]
	s_nop 0
	v_cvt_pk_fp8_f32 v114, v48, v49
	v_cvt_f32_i32_e32 v49, v111
	v_cvt_f32_i32_e32 v48, v110
	s_nop 0
	v_cvt_pk_fp8_f32 v115, v72, v73
	v_cvt_pk_fp8_f32 v114, v68, v69 op_sel:[0,0,1]
	v_pk_mul_f32 v[48:49], v[74:75], v[48:49]
	v_cvt_f32_i32_e32 v69, v107
	v_pk_fma_f32 v[48:49], v[48:49], v[222:223], v[70:71] op_sel_hi:[1,0,1]
	v_cvt_f32_i32_e32 v68, v106
	v_min_f32_e32 v48, 0x40e00000, v48
	v_min_f32_e32 v49, 0x40e00000, v49
	v_pk_mul_f32 v[72:73], v[48:49], s[12:13] op_sel_hi:[1,0]
	v_pk_mul_f32 v[68:69], v[78:79], v[68:69]
	v_exp_f32_e32 v72, v72
	v_exp_f32_e32 v73, v73
	v_pk_fma_f32 v[68:69], v[68:69], v[222:223], v[182:183] op_sel_hi:[1,0,1]
	v_cvt_pk_fp8_f32 v115, v116, v117 op_sel:[0,0,1]
	v_med3_f32 v68, v68, s54, v210
	v_pk_fma_f32 v[72:73], v[72:73], s[14:15], s[14:15] op_sel_hi:[1,0,0]
	v_med3_f32 v69, v69, s54, v210
	v_rcp_f32_e32 v72, v72
	v_rcp_f32_e32 v73, v73
	s_nop 0
	s_nop 0
	v_pk_mul_f32 v[48:49], v[48:49], v[72:73]
	s_nop 0
	v_pk_mul_f32 v[48:49], v[68:69], v[48:49]
	v_cvt_f32_i32_e32 v69, v113
	v_cvt_f32_i32_e32 v68, v112
	v_cvt_f32_i32_e32 v73, v109
	v_cvt_f32_i32_e32 v72, v108
	v_cvt_pk_fp8_f32 v116, v48, v49
	v_pk_mul_f32 v[68:69], v[76:77], v[68:69]
	v_or_b32_e32 v48, v45, v192
	v_pk_fma_f32 v[68:69], v[68:69], v[222:223], v[66:67] op_sel_hi:[1,0,1]
	v_pk_mul_f32 v[72:73], v[80:81], v[72:73]
	v_min_f32_e32 v68, 0x40e00000, v68
	v_min_f32_e32 v69, 0x40e00000, v69
	v_pk_mul_f32 v[106:107], v[68:69], s[12:13] op_sel_hi:[1,0]
	v_pk_fma_f32 v[72:73], v[72:73], v[222:223], v[180:181] op_sel_hi:[1,0,1]
	v_exp_f32_e32 v106, v106
	v_exp_f32_e32 v107, v107
	v_med3_f32 v72, v72, s54, v210
	v_med3_f32 v73, v73, s54, v210
	v_ashrrev_i32_e32 v49, 31, v48
	v_pk_fma_f32 v[106:107], v[106:107], s[14:15], s[14:15] op_sel_hi:[1,0,0]
	v_lshlrev_b64 v[48:49], 10, v[48:49]
	v_rcp_f32_e32 v106, v106
	v_rcp_f32_e32 v107, v107
	v_lshl_add_u64 v[48:49], s[94:95], 0, v[48:49]
	v_lshl_add_u64 v[48:49], v[48:49], 0, v[172:173]
	v_pk_mul_f32 v[68:69], v[68:69], v[106:107]
	s_nop 0
	v_pk_mul_f32 v[68:69], v[72:73], v[68:69]
	v_cvt_f32_i32_e32 v73, v103
	v_cvt_f32_i32_e32 v72, v102
	v_cvt_pk_fp8_f32 v116, v68, v69 op_sel:[0,0,1]
	v_cvt_f32_i32_e32 v69, v91
	v_cvt_f32_i32_e32 v68, v90
	v_pk_mul_f32 v[72:73], v[50:51], v[72:73]
	v_permlane16_swap_b32_e32 v114, v116
	v_pk_fma_f32 v[72:73], v[72:73], v[222:223], v[46:47] op_sel_hi:[1,0,1]
	v_pk_mul_f32 v[68:69], v[78:79], v[68:69]
	v_min_f32_e32 v72, 0x40e00000, v72
	v_min_f32_e32 v73, 0x40e00000, v73
	v_pk_mul_f32 v[102:103], v[72:73], s[12:13] op_sel_hi:[1,0]
	s_nop 0
	v_exp_f32_e32 v102, v102
	v_exp_f32_e32 v103, v103
	s_nop 0
	v_pk_fma_f32 v[102:103], v[102:103], s[14:15], s[14:15] op_sel_hi:[1,0,0]
	s_nop 0
	v_rcp_f32_e32 v102, v102
	v_rcp_f32_e32 v103, v103
	s_nop 0
	v_pk_mul_f32 v[72:73], v[72:73], v[102:103]
	s_nop 0
	v_pk_mul_f32 v[72:73], v[98:99], v[72:73]
	v_cvt_f32_i32_e32 v99, v105
	v_cvt_f32_i32_e32 v98, v104
	v_cvt_pk_fp8_f32 v117, v72, v73
	v_pk_mul_f32 v[98:99], v[52:53], v[98:99]
	s_nop 0
	v_pk_fma_f32 v[98:99], v[98:99], v[222:223], v[42:43] op_sel_hi:[1,0,1]
	v_add_u32_e32 v45, 0x80, v45
	v_min_f32_e32 v98, 0x40e00000, v98
	v_min_f32_e32 v99, 0x40e00000, v99
	v_pk_mul_f32 v[102:103], v[98:99], s[12:13] op_sel_hi:[1,0]
	s_nop 0
	v_exp_f32_e32 v102, v102
	v_exp_f32_e32 v103, v103
	s_nop 0
	v_pk_fma_f32 v[102:103], v[102:103], s[14:15], s[14:15] op_sel_hi:[1,0,0]
	s_nop 0
	v_rcp_f32_e32 v102, v102
	v_rcp_f32_e32 v103, v103
	s_nop 0
	v_pk_mul_f32 v[98:99], v[98:99], v[102:103]
	s_nop 0
	v_pk_mul_f32 v[98:99], v[100:101], v[98:99]
	s_nop 0
	v_cvt_pk_fp8_f32 v117, v98, v99 op_sel:[0,0,1]
	s_nop 1
	v_permlane16_swap_b32_e32 v115, v117
	global_store_dwordx4 v[48:49], v[114:117], off
	s_nop 0
	v_cvt_f32_i32_e32 v49, v95
	v_cvt_f32_i32_e32 v48, v94
	v_pk_mul_f32 v[48:49], v[74:75], v[48:49]
	s_waitcnt vmcnt(5)
	v_pk_fma_f32 v[48:49], v[48:49], v[224:225], v[70:71] op_sel_hi:[1,0,1]
	s_nop 0
	v_min_f32_e32 v48, 0x40e00000, v48
	v_min_f32_e32 v49, 0x40e00000, v49
	v_pk_mul_f32 v[72:73], v[48:49], s[12:13] op_sel_hi:[1,0]
	v_pk_fma_f32 v[68:69], v[68:69], v[224:225], v[182:183] op_sel_hi:[1,0,1]
	v_exp_f32_e32 v72, v72
	v_exp_f32_e32 v73, v73
	v_med3_f32 v68, v68, s54, v210
	v_med3_f32 v69, v69, s54, v210
	v_pk_fma_f32 v[82:83], v[82:83], v[224:225], v[178:179] op_sel_hi:[1,0,1]
	v_pk_fma_f32 v[72:73], v[72:73], s[14:15], s[14:15] op_sel_hi:[1,0,0]
	v_med3_f32 v82, v82, s54, v210
	v_rcp_f32_e32 v72, v72
	v_rcp_f32_e32 v73, v73
	v_med3_f32 v83, v83, s54, v210
	v_pk_fma_f32 v[84:85], v[84:85], v[224:225], v[176:177] op_sel_hi:[1,0,1]
	v_pk_mul_f32 v[48:49], v[48:49], v[72:73]
	s_nop 0
	v_pk_mul_f32 v[48:49], v[68:69], v[48:49]
	v_cvt_f32_i32_e32 v69, v97
	v_cvt_f32_i32_e32 v68, v96
	v_cvt_f32_i32_e32 v73, v93
	v_cvt_f32_i32_e32 v72, v92
	v_med3_f32 v84, v84, s54, v210
	v_pk_mul_f32 v[68:69], v[76:77], v[68:69]
	v_med3_f32 v85, v85, s54, v210
	v_pk_fma_f32 v[68:69], v[68:69], v[224:225], v[66:67] op_sel_hi:[1,0,1]
	v_pk_mul_f32 v[72:73], v[80:81], v[72:73]
	v_min_f32_e32 v68, 0x40e00000, v68
	v_min_f32_e32 v69, 0x40e00000, v69
	v_pk_mul_f32 v[90:91], v[68:69], s[12:13] op_sel_hi:[1,0]
	v_pk_fma_f32 v[72:73], v[72:73], v[224:225], v[180:181] op_sel_hi:[1,0,1]
	v_exp_f32_e32 v90, v90
	v_exp_f32_e32 v91, v91
	v_med3_f32 v72, v72, s54, v210
	v_med3_f32 v73, v73, s54, v210
	v_pk_fma_f32 v[90:91], v[90:91], s[14:15], s[14:15] op_sel_hi:[1,0,0]
	s_nop 0
	v_rcp_f32_e32 v90, v90
	v_rcp_f32_e32 v91, v91
	s_nop 0
	v_pk_mul_f32 v[68:69], v[68:69], v[90:91]
	s_nop 0
	v_pk_mul_f32 v[68:69], v[72:73], v[68:69]
	v_cvt_f32_i32_e32 v73, v87
	v_cvt_f32_i32_e32 v72, v86
	v_pk_mul_f32 v[72:73], v[50:51], v[72:73]
	s_nop 0
	v_pk_fma_f32 v[72:73], v[72:73], v[224:225], v[46:47] op_sel_hi:[1,0,1]
	s_nop 0
	v_min_f32_e32 v72, 0x40e00000, v72
	v_min_f32_e32 v73, 0x40e00000, v73
	v_pk_mul_f32 v[86:87], v[72:73], s[12:13] op_sel_hi:[1,0]
	s_nop 0
	v_exp_f32_e32 v86, v86
	v_exp_f32_e32 v87, v87
	s_nop 0
	v_pk_fma_f32 v[86:87], v[86:87], s[14:15], s[14:15] op_sel_hi:[1,0,0]
	s_nop 0
	v_rcp_f32_e32 v86, v86
	v_rcp_f32_e32 v87, v87
	s_nop 0
	v_pk_mul_f32 v[72:73], v[72:73], v[86:87]
	s_nop 0
	v_pk_mul_f32 v[72:73], v[82:83], v[72:73]
	v_cvt_f32_i32_e32 v83, v89
	v_cvt_f32_i32_e32 v82, v88
	v_pk_mul_f32 v[82:83], v[52:53], v[82:83]
	s_nop 0
	v_pk_fma_f32 v[82:83], v[82:83], v[224:225], v[42:43] op_sel_hi:[1,0,1]
	s_nop 0
	v_min_f32_e32 v82, 0x40e00000, v82
	v_min_f32_e32 v83, 0x40e00000, v83
	v_pk_mul_f32 v[86:87], v[82:83], s[12:13] op_sel_hi:[1,0]
	s_waitcnt vmcnt(4)
	v_pk_fma_f32 v[58:59], v[58:59], v[226:227], v[182:183] op_sel_hi:[1,0,1]
	v_exp_f32_e32 v86, v86
	v_exp_f32_e32 v87, v87
	v_med3_f32 v58, v58, s54, v210
	v_med3_f32 v59, v59, s54, v210
	v_pk_fma_f32 v[60:61], v[60:61], v[226:227], v[180:181] op_sel_hi:[1,0,1]
	v_pk_fma_f32 v[86:87], v[86:87], s[14:15], s[14:15] op_sel_hi:[1,0,0]
	v_pk_fma_f32 v[38:39], v[38:39], v[226:227], v[46:47] op_sel_hi:[1,0,1]
	v_rcp_f32_e32 v86, v86
	v_rcp_f32_e32 v87, v87
	v_med3_f32 v60, v60, s54, v210
	v_med3_f32 v61, v61, s54, v210
	v_min_f32_e32 v38, 0x40e00000, v38
	v_pk_mul_f32 v[82:83], v[82:83], v[86:87]
	v_min_f32_e32 v39, 0x40e00000, v39
	v_pk_mul_f32 v[84:85], v[84:85], v[82:83]
	s_nop 0
	v_cvt_pk_fp8_f32 v82, v48, v49
	v_cvt_f32_i32_e32 v49, v63
	v_cvt_f32_i32_e32 v48, v62
	v_pk_fma_f32 v[22:23], v[22:23], v[226:227], v[178:179] op_sel_hi:[1,0,1]
	s_nop 0
	v_med3_f32 v22, v22, s54, v210
	v_pk_mul_f32 v[48:49], v[74:75], v[48:49]
	v_med3_f32 v23, v23, s54, v210
	v_pk_fma_f32 v[48:49], v[48:49], v[226:227], v[70:71] op_sel_hi:[1,0,1]
	v_cvt_pk_fp8_f32 v83, v72, v73
	v_min_f32_e32 v48, 0x40e00000, v48
	v_min_f32_e32 v49, 0x40e00000, v49
	v_pk_mul_f32 v[62:63], v[48:49], s[12:13] op_sel_hi:[1,0]
	v_cvt_pk_fp8_f32 v83, v84, v85 op_sel:[0,0,1]
	v_exp_f32_e32 v62, v62
	v_exp_f32_e32 v63, v63
	s_nop 0
	s_nop 0
	v_pk_fma_f32 v[24:25], v[24:25], v[226:227], v[176:177] op_sel_hi:[1,0,1]
	v_pk_fma_f32 v[62:63], v[62:63], s[14:15], s[14:15] op_sel_hi:[1,0,0]
	v_med3_f32 v24, v24, s54, v210
	v_rcp_f32_e32 v62, v62
	v_rcp_f32_e32 v63, v63
	v_med3_f32 v25, v25, s54, v210
	v_cvt_pk_fp8_f32 v82, v68, v69 op_sel:[0,0,1]
	v_pk_mul_f32 v[48:49], v[48:49], v[62:63]
	s_nop 0
	v_pk_mul_f32 v[48:49], v[58:59], v[48:49]
	v_cvt_f32_i32_e32 v59, v65
	v_cvt_f32_i32_e32 v58, v64
	v_cvt_pk_fp8_f32 v84, v48, v49
	v_pk_mul_f32 v[58:59], v[76:77], v[58:59]
	s_nop 0
	v_pk_fma_f32 v[58:59], v[58:59], v[226:227], v[66:67] op_sel_hi:[1,0,1]
	s_nop 0
	v_min_f32_e32 v58, 0x40e00000, v58
	v_min_f32_e32 v59, 0x40e00000, v59
	v_pk_mul_f32 v[62:63], v[58:59], s[12:13] op_sel_hi:[1,0]
	s_nop 0
	v_exp_f32_e32 v62, v62
	v_exp_f32_e32 v63, v63
	s_nop 0
	v_pk_fma_f32 v[62:63], v[62:63], s[14:15], s[14:15] op_sel_hi:[1,0,0]
	s_nop 0
	v_rcp_f32_e32 v62, v62
	v_rcp_f32_e32 v63, v63
	s_nop 0
	v_pk_mul_f32 v[58:59], v[58:59], v[62:63]
	s_nop 0
	v_pk_mul_f32 v[58:59], v[60:61], v[58:59]
	v_pk_mul_f32 v[60:61], v[38:39], s[12:13] op_sel_hi:[1,0]
	v_cvt_pk_fp8_f32 v84, v58, v59 op_sel:[0,0,1]
	v_exp_f32_e32 v60, v60
	v_exp_f32_e32 v61, v61
	v_permlane16_swap_b32_e32 v82, v84
	v_pk_fma_f32 v[60:61], v[60:61], s[14:15], s[14:15] op_sel_hi:[1,0,0]
	s_nop 0
	v_rcp_f32_e32 v60, v60
	v_rcp_f32_e32 v61, v61
	s_nop 0
	v_pk_mul_f32 v[38:39], v[38:39], v[60:61]
	s_nop 0
	v_pk_mul_f32 v[22:23], v[22:23], v[38:39]
	v_cvt_f32_i32_e32 v39, v41
	v_cvt_f32_i32_e32 v38, v40
	v_cvt_pk_fp8_f32 v85, v22, v23
	v_or_b32_e32 v22, v45, v191
	v_ashrrev_i32_e32 v23, 31, v22
	v_pk_mul_f32 v[38:39], v[52:53], v[38:39]
	v_lshlrev_b64 v[22:23], 10, v[22:23]
	v_pk_fma_f32 v[38:39], v[38:39], v[226:227], v[42:43] op_sel_hi:[1,0,1]
	v_lshl_add_u64 v[22:23], s[94:95], 0, v[22:23]
	v_min_f32_e32 v38, 0x40e00000, v38
	v_min_f32_e32 v39, 0x40e00000, v39
	v_pk_mul_f32 v[40:41], v[38:39], s[12:13] op_sel_hi:[1,0]
	v_lshl_add_u64 v[22:23], v[22:23], 0, v[172:173]
	v_exp_f32_e32 v40, v40
	v_exp_f32_e32 v41, v41
	s_nop 0
	v_pk_fma_f32 v[40:41], v[40:41], s[14:15], s[14:15] op_sel_hi:[1,0,0]
	s_nop 0
	v_rcp_f32_e32 v40, v40
	v_rcp_f32_e32 v41, v41
	s_nop 0
	v_pk_mul_f32 v[38:39], v[38:39], v[40:41]
	s_nop 0
	v_pk_mul_f32 v[24:25], v[24:25], v[38:39]
	s_nop 0
	v_cvt_pk_fp8_f32 v85, v24, v25 op_sel:[0,0,1]
	v_cvt_f32_i32_e32 v25, v27
	v_cvt_f32_i32_e32 v24, v26
	v_cvt_f32_i32_e32 v27, v35
	v_permlane16_swap_b32_e32 v83, v85
	global_store_dwordx4 v[22:23], v[82:85], off
	s_nop 0
	v_pk_mul_f32 v[24:25], v[74:75], v[24:25]
	v_cvt_f32_i32_e32 v26, v34
	v_pk_mul_f32 v[26:27], v[78:79], v[26:27]
	s_waitcnt vmcnt(4)
	v_pk_fma_f32 v[24:25], v[24:25], v[228:229], v[70:71] op_sel_hi:[1,0,1]
	s_nop 0
	v_min_f32_e32 v24, 0x40e00000, v24
	v_min_f32_e32 v25, 0x40e00000, v25
	v_pk_mul_f32 v[34:35], v[24:25], s[12:13] op_sel_hi:[1,0]
	v_pk_fma_f32 v[26:27], v[26:27], v[228:229], v[182:183] op_sel_hi:[1,0,1]
	v_exp_f32_e32 v34, v34
	v_exp_f32_e32 v35, v35
	v_med3_f32 v26, v26, s54, v210
	v_med3_f32 v27, v27, s54, v210
	v_pk_fma_f32 v[18:19], v[18:19], v[228:229], v[46:47] op_sel_hi:[1,0,1]
	v_pk_fma_f32 v[34:35], v[34:35], s[14:15], s[14:15] op_sel_hi:[1,0,0]
	v_min_f32_e32 v18, 0x40e00000, v18
	v_rcp_f32_e32 v34, v34
	v_rcp_f32_e32 v35, v35
	v_min_f32_e32 v19, 0x40e00000, v19
	v_pk_mul_f32 v[24:25], v[24:25], v[34:35]
	s_nop 0
	v_pk_mul_f32 v[24:25], v[26:27], v[24:25]
	v_cvt_f32_i32_e32 v27, v29
	v_cvt_f32_i32_e32 v26, v28
	v_cvt_f32_i32_e32 v29, v37
	v_cvt_f32_i32_e32 v28, v36
	v_pk_mul_f32 v[26:27], v[76:77], v[26:27]
	s_nop 0
	v_pk_fma_f32 v[26:27], v[26:27], v[228:229], v[66:67] op_sel_hi:[1,0,1]
	v_pk_mul_f32 v[28:29], v[80:81], v[28:29]
	v_min_f32_e32 v26, 0x40e00000, v26
	v_min_f32_e32 v27, 0x40e00000, v27
	v_pk_mul_f32 v[34:35], v[26:27], s[12:13] op_sel_hi:[1,0]
	v_pk_fma_f32 v[28:29], v[28:29], v[228:229], v[180:181] op_sel_hi:[1,0,1]
	v_exp_f32_e32 v34, v34
	v_exp_f32_e32 v35, v35
	v_med3_f32 v28, v28, s54, v210
	v_med3_f32 v29, v29, s54, v210
	v_pk_fma_f32 v[34:35], v[34:35], s[14:15], s[14:15] op_sel_hi:[1,0,0]
	s_nop 0
	v_rcp_f32_e32 v34, v34
	v_rcp_f32_e32 v35, v35
	s_nop 0
	v_pk_mul_f32 v[26:27], v[26:27], v[34:35]
	s_nop 0
	v_pk_mul_f32 v[26:27], v[28:29], v[26:27]
	v_cvt_f32_i32_e32 v29, v31
	v_cvt_f32_i32_e32 v28, v30
	v_pk_mul_f32 v[30:31], v[18:19], s[12:13] op_sel_hi:[1,0]
	v_pk_mul_f32 v[28:29], v[54:55], v[28:29]
	v_exp_f32_e32 v30, v30
	v_exp_f32_e32 v31, v31
	v_pk_fma_f32 v[28:29], v[28:29], v[228:229], v[178:179] op_sel_hi:[1,0,1]
	v_pk_fma_f32 v[30:31], v[30:31], s[14:15], s[14:15] op_sel_hi:[1,0,0]
	s_nop 0
	v_rcp_f32_e32 v30, v30
	v_rcp_f32_e32 v31, v31
	v_med3_f32 v28, v28, s54, v210
	v_med3_f32 v29, v29, s54, v210
	v_pk_mul_f32 v[18:19], v[18:19], v[30:31]
	s_nop 0
	v_pk_mul_f32 v[28:29], v[28:29], v[18:19]
	v_cvt_f32_i32_e32 v19, v21
	v_cvt_f32_i32_e32 v18, v20
	v_cvt_f32_i32_e32 v21, v33
	v_cvt_f32_i32_e32 v20, v32
	v_pk_mul_f32 v[18:19], v[52:53], v[18:19]
	s_nop 0
	v_pk_fma_f32 v[18:19], v[18:19], v[228:229], v[42:43] op_sel_hi:[1,0,1]
	v_pk_mul_f32 v[20:21], v[56:57], v[20:21]
	v_min_f32_e32 v18, 0x40e00000, v18
	v_min_f32_e32 v19, 0x40e00000, v19
	v_pk_fma_f32 v[20:21], v[20:21], v[228:229], v[176:177] op_sel_hi:[1,0,1]
	v_pk_mul_f32 v[22:23], v[18:19], s[12:13] op_sel_hi:[1,0]
	v_med3_f32 v20, v20, s54, v210
	v_exp_f32_e32 v22, v22
	v_exp_f32_e32 v23, v23
	v_med3_f32 v21, v21, s54, v210
	v_pk_fma_f32 v[22:23], v[22:23], s[14:15], s[14:15] op_sel_hi:[1,0,0]
	s_nop 0
	v_rcp_f32_e32 v22, v22
	v_rcp_f32_e32 v23, v23
	s_nop 0
	v_pk_mul_f32 v[18:19], v[18:19], v[22:23]
	s_nop 0
	v_pk_mul_f32 v[20:21], v[20:21], v[18:19]
	s_nop 0
	v_cvt_pk_fp8_f32 v19, v28, v29
	s_nop 0
	v_cvt_pk_fp8_f32 v18, v24, v25
	v_cvt_pk_fp8_f32 v19, v20, v21 op_sel:[0,0,1]
	s_nop 0
	v_cvt_pk_fp8_f32 v18, v26, v27 op_sel:[0,0,1]
	s_waitcnt vmcnt(3)
	v_pk_fma_f32 v[10:11], v[10:11], v[230:231], v[70:71] op_sel_hi:[1,0,1]
	s_nop 0
	v_min_f32_e32 v10, 0x40e00000, v10
	v_min_f32_e32 v11, 0x40e00000, v11
	v_pk_mul_f32 v[22:23], v[10:11], s[12:13] op_sel_hi:[1,0]
	v_pk_fma_f32 v[14:15], v[14:15], v[230:231], v[182:183] op_sel_hi:[1,0,1]
	v_exp_f32_e32 v22, v22
	v_exp_f32_e32 v23, v23
	v_pk_fma_f32 v[12:13], v[12:13], v[230:231], v[66:67] op_sel_hi:[1,0,1]
	v_med3_f32 v14, v14, s54, v210
	v_med3_f32 v15, v15, s54, v210
	v_pk_fma_f32 v[22:23], v[22:23], s[14:15], s[14:15] op_sel_hi:[1,0,0]
	v_min_f32_e32 v12, 0x40e00000, v12
	v_rcp_f32_e32 v22, v22
	v_rcp_f32_e32 v23, v23
	v_min_f32_e32 v13, 0x40e00000, v13
	v_pk_fma_f32 v[2:3], v[2:3], v[230:231], v[46:47] op_sel_hi:[1,0,1]
	v_pk_fma_f32 v[6:7], v[6:7], v[230:231], v[178:179] op_sel_hi:[1,0,1]
	v_pk_mul_f32 v[10:11], v[10:11], v[22:23]
	v_min_f32_e32 v2, 0x40e00000, v2
	v_pk_mul_f32 v[10:11], v[14:15], v[10:11]
	v_cvt_f32_i32_e32 v15, v17
	v_cvt_f32_i32_e32 v14, v16
	v_pk_mul_f32 v[16:17], v[12:13], s[12:13] op_sel_hi:[1,0]
	v_min_f32_e32 v3, 0x40e00000, v3
	v_exp_f32_e32 v16, v16
	v_exp_f32_e32 v17, v17
	v_pk_mul_f32 v[14:15], v[80:81], v[14:15]
	v_pk_fma_f32 v[4:5], v[4:5], v[230:231], v[42:43] op_sel_hi:[1,0,1]
	v_pk_fma_f32 v[14:15], v[14:15], v[230:231], v[180:181] op_sel_hi:[1,0,1]
	v_pk_fma_f32 v[16:17], v[16:17], s[14:15], s[14:15] op_sel_hi:[1,0,0]
	v_med3_f32 v14, v14, s54, v210
	v_rcp_f32_e32 v16, v16
	v_rcp_f32_e32 v17, v17
	v_med3_f32 v15, v15, s54, v210
	v_med3_f32 v6, v6, s54, v210
	v_med3_f32 v7, v7, s54, v210
	v_pk_mul_f32 v[12:13], v[12:13], v[16:17]
	v_min_f32_e32 v4, 0x40e00000, v4
	v_pk_mul_f32 v[12:13], v[14:15], v[12:13]
	v_pk_mul_f32 v[14:15], v[2:3], s[12:13] op_sel_hi:[1,0]
	v_min_f32_e32 v5, 0x40e00000, v5
	v_exp_f32_e32 v14, v14
	v_exp_f32_e32 v15, v15
	s_nop 0
	v_pk_fma_f32 v[14:15], v[14:15], s[14:15], s[14:15] op_sel_hi:[1,0,0]
	s_nop 0
	v_rcp_f32_e32 v14, v14
	v_rcp_f32_e32 v15, v15
	s_nop 0
	v_pk_mul_f32 v[2:3], v[2:3], v[14:15]
	s_nop 0
	v_pk_mul_f32 v[2:3], v[6:7], v[2:3]
	v_cvt_f32_i32_e32 v7, v9
	v_cvt_f32_i32_e32 v6, v8
	v_pk_mul_f32 v[8:9], v[4:5], s[12:13] op_sel_hi:[1,0]
	v_pk_mul_f32 v[6:7], v[56:57], v[6:7]
	v_exp_f32_e32 v8, v8
	v_exp_f32_e32 v9, v9
	v_pk_fma_f32 v[6:7], v[6:7], v[230:231], v[176:177] op_sel_hi:[1,0,1]
	s_nop 0
	s_nop 0
	v_pk_fma_f32 v[8:9], v[8:9], s[14:15], s[14:15] op_sel_hi:[1,0,0]
	v_cvt_pk_fp8_f32 v20, v10, v11
	v_rcp_f32_e32 v8, v8
	v_rcp_f32_e32 v9, v9
	v_cvt_pk_fp8_f32 v21, v2, v3
	v_med3_f32 v6, v6, s54, v210
	v_med3_f32 v7, v7, s54, v210
	v_pk_mul_f32 v[4:5], v[4:5], v[8:9]
	v_cvt_pk_fp8_f32 v20, v12, v13 op_sel:[0,0,1]
	v_pk_mul_f32 v[4:5], v[6:7], v[4:5]
	v_or_b32_e32 v2, v45, v192
	v_cvt_pk_fp8_f32 v21, v4, v5 op_sel:[0,0,1]
	v_ashrrev_i32_e32 v3, 31, v2
	v_lshlrev_b64 v[2:3], 10, v[2:3]
	v_lshl_add_u64 v[2:3], s[94:95], 0, v[2:3]
	v_permlane16_swap_b32_e32 v18, v20
	v_permlane16_swap_b32_e32 v19, v21
	v_lshl_add_u64 v[2:3], v[2:3], 0, v[172:173]
	global_store_dwordx4 v[2:3], v[18:21], off
	s_cbranch_vccnz .LBB0_497
	s_andn2_b64 vcc, exec, s[4:5]
	s_cbranch_vccnz .LBB0_496
	s_barrier
	s_branch .LBB0_496

.LBB0_590:
	s_lshl_b32 s1, s40, 2
	s_add_i32 s1, s1, 0
	s_nop 15
	s_nop 15
	s_add_i32 s1, s1, 0x20480
	v_mov_b32_e32 v2, s1
	ds_read_b32 v2, v2
	s_ashr_i32 s41, s40, 31
	s_lshl_b64 s[18:19], s[40:41], 18
	s_add_u32 s18, s78, s18
	s_addc_u32 s19, s79, s19
	s_waitcnt lgkmcnt(0)
	v_sub_u32_e32 v2, s26, v2
	v_lshl_add_u32 v2, v2, 8, v1
	v_ashrrev_i32_e32 v3, 31, v2
	v_lshl_add_u64 v[2:3], v[2:3], 2, s[18:19]
	global_load_dword v28, v[2:3], off
	global_load_dword v26, v[2:3], off offset:64
	global_load_dword v24, v[2:3], off offset:128
	global_load_dword v22, v[2:3], off offset:192
	global_load_dword v20, v[2:3], off offset:512
	global_load_dword v18, v[2:3], off offset:576
	global_load_dword v16, v[2:3], off offset:640
	global_load_dword v14, v[2:3], off offset:704
	v_readlane_b32 s84, v252, 0
	v_readlane_b32 s88, v252, 4
	v_readlane_b32 s89, v252, 5
	s_lshl_b64 s[18:19], s[40:41], 12
	v_readlane_b32 s90, v252, 6
	v_readlane_b32 s91, v252, 7
	s_mov_b64 s[40:41], s[88:89]
	s_add_u32 s22, s40, s18
	s_addc_u32 s23, s41, s19
	s_add_u32 s18, s48, s18
	s_addc_u32 s19, s49, s19
	v_lshl_add_u32 v15, s26, 8, v1
	s_andn2_b64 vcc, exec, s[14:15]
	v_readlane_b32 s85, v252, 1
	v_readlane_b32 s86, v252, 2
	v_readlane_b32 s87, v252, 3
	s_mov_b64 s[42:43], s[90:91]
	v_lshl_or_b32 v2, s28, 8, v209
	v_ashrrev_i32_e32 v3, 31, v2
	v_sub_u32_e32 v30, v2, v190
	v_lshlrev_b64 v[2:3], 2, v[2:3]
	v_lshl_add_u64 v[180:181], s[22:23], 0, v[2:3]
	v_lshl_add_u64 v[32:33], s[18:19], 0, v[2:3]
	global_load_dwordx4 v[2:5], v[180:181], off offset:16
	global_load_dwordx4 v[6:9], v[180:181], off
	global_load_dwordx4 v[10:13], v[32:33], off offset:16
	global_load_dwordx4 v[182:185], v[32:33], off
	s_waitcnt vmcnt(0)
	v_mul_f32_e32 v28, 4.0, v28
	v_mul_f32_e32 v26, 4.0, v26
	v_mul_f32_e32 v24, 4.0, v24
	v_mul_f32_e32 v22, 4.0, v22
	v_mul_f32_e32 v20, 4.0, v20
	v_mul_f32_e32 v18, 4.0, v18
	v_mul_f32_e32 v16, 4.0, v16
	v_mul_f32_e32 v14, 4.0, v14
	v_ashrrev_i32_e32 v31, 31, v30
	s_mov_b64 s[18:19], -1
	s_waitcnt vmcnt(0)
	v_pk_mul_f32 v[186:187], v[184:185], s[8:9] op_sel_hi:[1,0]
	v_pk_mul_f32 v[188:189], v[182:183], s[8:9] op_sel_hi:[1,0]
	v_pk_mul_f32 v[182:183], v[12:13], s[8:9] op_sel_hi:[1,0]
	v_pk_mul_f32 v[184:185], v[10:11], s[8:9] op_sel_hi:[1,0]
	v_pk_fma_f32 v[10:11], v[160:161], v[186:187], v[8:9]
	v_pk_fma_f32 v[12:13], v[158:159], v[188:189], v[6:7]
	v_pk_mul_f32 v[158:159], v[28:29], v[10:11] op_sel_hi:[0,1]
	v_pk_mul_f32 v[12:13], v[28:29], v[12:13] op_sel_hi:[0,1]
	v_pk_fma_f32 v[10:11], v[156:157], v[182:183], v[4:5]
	v_pk_fma_f32 v[154:155], v[154:155], v[184:185], v[2:3]
	v_pk_mul_f32 v[156:157], v[28:29], v[10:11] op_sel_hi:[0,1]
	v_med3_f32 v11, v12, s56, v212
	v_med3_f32 v12, v13, s56, v212
	s_nop 0
	v_cvt_pk_fp8_f32 v10, v11, v12
	v_pk_mul_f32 v[154:155], v[28:29], v[154:155] op_sel_hi:[0,1]
	v_med3_f32 v11, v158, s56, v212
	v_med3_f32 v12, v159, s56, v212
	v_cvt_pk_fp8_f32 v10, v11, v12 op_sel:[0,0,1]
	v_med3_f32 v12, v154, s56, v212
	v_med3_f32 v13, v155, s56, v212
	s_nop 0
	v_cvt_pk_fp8_f32 v11, v12, v13
	v_med3_f32 v12, v156, s56, v212
	v_med3_f32 v13, v157, s56, v212
	v_pk_fma_f32 v[150:151], v[150:151], v[188:189], v[6:7]
	v_cvt_pk_fp8_f32 v11, v12, v13 op_sel:[0,0,1]
	v_pk_fma_f32 v[12:13], v[152:153], v[186:187], v[8:9]
	v_pk_mul_f32 v[150:151], v[26:27], v[150:151] op_sel_hi:[0,1]
	v_pk_mul_f32 v[152:153], v[26:27], v[12:13] op_sel_hi:[0,1]
	v_pk_fma_f32 v[12:13], v[148:149], v[182:183], v[4:5]
	v_med3_f32 v17, v151, s56, v212
	v_pk_mul_f32 v[148:149], v[26:27], v[12:13] op_sel_hi:[0,1]
	v_med3_f32 v13, v150, s56, v212
	s_nop 0
	v_cvt_pk_fp8_f32 v12, v13, v17
	v_pk_fma_f32 v[146:147], v[146:147], v[184:185], v[2:3]
	v_med3_f32 v13, v152, s56, v212
	v_pk_mul_f32 v[146:147], v[26:27], v[146:147] op_sel_hi:[0,1]
	v_med3_f32 v17, v153, s56, v212
	v_cvt_pk_fp8_f32 v12, v13, v17 op_sel:[0,0,1]
	v_med3_f32 v17, v146, s56, v212
	v_med3_f32 v19, v147, s56, v212
	s_nop 0
	v_cvt_pk_fp8_f32 v13, v17, v19
	v_med3_f32 v17, v148, s56, v212
	v_med3_f32 v19, v149, s56, v212
	v_or_b32_e32 v146, v15, v191
	v_cvt_pk_fp8_f32 v13, v17, v19 op_sel:[0,0,1]
	v_ashrrev_i32_e32 v147, 31, v146
	v_lshlrev_b64 v[146:147], 10, v[146:147]
	v_lshl_add_u64 v[146:147], s[92:93], 0, v[146:147]
	v_permlane16_swap_b32_e32 v10, v12
	v_permlane16_swap_b32_e32 v11, v13
	v_lshl_add_u64 v[146:147], v[146:147], 0, v[30:31]
	global_store_dwordx4 v[146:147], v[10:13], off
	v_pk_fma_f32 v[138:139], v[138:139], v[184:185], v[2:3]
	v_pk_fma_f32 v[140:141], v[140:141], v[182:183], v[4:5]
	v_pk_fma_f32 v[12:13], v[142:143], v[188:189], v[6:7]
	v_pk_mul_f32 v[142:143], v[24:25], v[138:139] op_sel_hi:[0,1]
	v_pk_mul_f32 v[12:13], v[24:25], v[12:13] op_sel_hi:[0,1]
	v_med3_f32 v12, v12, s56, v212
	v_med3_f32 v13, v13, s56, v212
	s_nop 0
	v_cvt_pk_fp8_f32 v138, v12, v13
	v_pk_fma_f32 v[10:11], v[144:145], v[186:187], v[8:9]
	v_pk_fma_f32 v[12:13], v[134:135], v[188:189], v[6:7]
	v_pk_mul_f32 v[10:11], v[24:25], v[10:11] op_sel_hi:[0,1]
	v_med3_f32 v10, v10, s56, v212
	v_med3_f32 v11, v11, s56, v212
	v_pk_mul_f32 v[140:141], v[24:25], v[140:141] op_sel_hi:[0,1]
	v_cvt_pk_fp8_f32 v138, v10, v11 op_sel:[0,0,1]
	v_med3_f32 v10, v142, s56, v212
	v_med3_f32 v11, v143, s56, v212
	s_nop 0
	v_pk_mul_f32 v[12:13], v[22:23], v[12:13] op_sel_hi:[0,1]
	v_pk_fma_f32 v[126:127], v[126:127], v[188:189], v[6:7]
	v_cvt_pk_fp8_f32 v139, v10, v11
	v_med3_f32 v10, v140, s56, v212
	v_med3_f32 v12, v12, s56, v212
	v_med3_f32 v13, v13, s56, v212
	s_nop 0
	v_pk_mul_f32 v[126:127], v[20:21], v[126:127] op_sel_hi:[0,1]
	v_pk_fma_f32 v[122:123], v[122:123], v[184:185], v[2:3]
	v_cvt_pk_fp8_f32 v140, v12, v13
	v_pk_fma_f32 v[12:13], v[128:129], v[186:187], v[8:9]
	v_pk_mul_f32 v[128:129], v[20:21], v[122:123] op_sel_hi:[0,1]
	v_med3_f32 v17, v126, s56, v212
	v_med3_f32 v19, v127, s56, v212
	s_nop 0
	v_cvt_pk_fp8_f32 v122, v17, v19
	v_pk_mul_f32 v[12:13], v[20:21], v[12:13] op_sel_hi:[0,1]
	v_med3_f32 v12, v12, s56, v212
	v_med3_f32 v13, v13, s56, v212
	v_cvt_pk_fp8_f32 v122, v12, v13 op_sel:[0,0,1]
	v_med3_f32 v12, v128, s56, v212
	v_med3_f32 v13, v129, s56, v212
	s_nop 0
	v_cvt_pk_fp8_f32 v123, v12, v13
	v_pk_fma_f32 v[124:125], v[124:125], v[182:183], v[4:5]
	v_pk_fma_f32 v[118:119], v[118:119], v[188:189], v[6:7]
	v_pk_mul_f32 v[124:125], v[20:21], v[124:125] op_sel_hi:[0,1]
	v_med3_f32 v12, v124, s56, v212
	v_med3_f32 v13, v125, s56, v212
	v_cvt_pk_fp8_f32 v123, v12, v13 op_sel:[0,0,1]
	v_pk_fma_f32 v[12:13], v[120:121], v[186:187], v[8:9]
	v_pk_mul_f32 v[118:119], v[18:19], v[118:119] op_sel_hi:[0,1]
	v_pk_fma_f32 v[116:117], v[116:117], v[182:183], v[4:5]
	v_pk_fma_f32 v[114:115], v[114:115], v[184:185], v[2:3]
	v_med3_f32 v11, v141, s56, v212
	v_pk_mul_f32 v[12:13], v[18:19], v[12:13] op_sel_hi:[0,1]
	v_pk_mul_f32 v[114:115], v[18:19], v[114:115] op_sel_hi:[0,1]
	v_pk_mul_f32 v[116:117], v[18:19], v[116:117] op_sel_hi:[0,1]
	v_med3_f32 v17, v118, s56, v212
	v_med3_f32 v19, v119, s56, v212
	s_nop 0
	v_cvt_pk_fp8_f32 v139, v10, v11 op_sel:[0,0,1]
	v_pk_fma_f32 v[10:11], v[136:137], v[186:187], v[8:9]
	v_cvt_pk_fp8_f32 v124, v17, v19
	v_pk_mul_f32 v[10:11], v[22:23], v[10:11] op_sel_hi:[0,1]
	v_pk_fma_f32 v[130:131], v[130:131], v[184:185], v[2:3]
	v_med3_f32 v10, v10, s56, v212
	v_pk_mul_f32 v[130:131], v[22:23], v[130:131] op_sel_hi:[0,1]
	v_med3_f32 v11, v11, s56, v212
	v_pk_fma_f32 v[110:111], v[110:111], v[188:189], v[6:7]
	v_cvt_pk_fp8_f32 v140, v10, v11 op_sel:[0,0,1]
	v_med3_f32 v10, v130, s56, v212
	v_med3_f32 v11, v131, s56, v212
	s_nop 0
	v_med3_f32 v12, v12, s56, v212
	v_med3_f32 v13, v13, s56, v212
	v_pk_fma_f32 v[112:113], v[112:113], v[186:187], v[8:9]
	v_pk_mul_f32 v[110:111], v[16:17], v[110:111] op_sel_hi:[0,1]
	v_pk_fma_f32 v[108:109], v[108:109], v[182:183], v[4:5]
	v_pk_fma_f32 v[106:107], v[106:107], v[184:185], v[2:3]
	v_cvt_pk_fp8_f32 v141, v10, v11
	v_cvt_pk_fp8_f32 v124, v12, v13 op_sel:[0,0,1]
	v_med3_f32 v12, v114, s56, v212
	v_med3_f32 v13, v115, s56, v212
	v_pk_mul_f32 v[112:113], v[16:17], v[112:113] op_sel_hi:[0,1]
	v_pk_mul_f32 v[114:115], v[16:17], v[106:107] op_sel_hi:[0,1]
	v_pk_mul_f32 v[108:109], v[16:17], v[108:109] op_sel_hi:[0,1]
	v_med3_f32 v17, v110, s56, v212
	v_med3_f32 v19, v111, s56, v212
	s_nop 0
	v_pk_fma_f32 v[132:133], v[132:133], v[182:183], v[4:5]
	v_cvt_pk_fp8_f32 v106, v17, v19
	v_pk_mul_f32 v[132:133], v[22:23], v[132:133] op_sel_hi:[0,1]
	v_med3_f32 v10, v132, s56, v212
	v_med3_f32 v11, v133, s56, v212
	v_cvt_pk_fp8_f32 v141, v10, v11 op_sel:[0,0,1]
	v_or_b32_e32 v10, v15, v192
	v_add_u32_e32 v15, 0x80, v15
	v_med3_f32 v17, v112, s56, v212
	v_med3_f32 v19, v113, s56, v212
	v_pk_fma_f32 v[6:7], v[102:103], v[188:189], v[6:7]
	v_pk_fma_f32 v[2:3], v[98:99], v[184:185], v[2:3]
	v_cvt_pk_fp8_f32 v106, v17, v19 op_sel:[0,0,1]
	v_med3_f32 v17, v114, s56, v212
	v_med3_f32 v19, v115, s56, v212
	s_nop 0
	v_pk_mul_f32 v[6:7], v[14:15], v[6:7] op_sel_hi:[0,1]
	v_pk_mul_f32 v[2:3], v[14:15], v[2:3] op_sel_hi:[0,1]
	s_nop 0
	v_cvt_pk_fp8_f32 v107, v17, v19
	v_med3_f32 v17, v108, s56, v212
	v_med3_f32 v19, v109, s56, v212
	v_med3_f32 v6, v6, s56, v212
	v_med3_f32 v7, v7, s56, v212
	s_nop 0
	v_med3_f32 v2, v2, s56, v212
	v_med3_f32 v3, v3, s56, v212
	s_nop 0
	v_cvt_pk_fp8_f32 v125, v12, v13
	v_cvt_pk_fp8_f32 v108, v6, v7
	v_cvt_pk_fp8_f32 v109, v2, v3
	v_pk_fma_f32 v[8:9], v[104:105], v[186:187], v[8:9]
	v_pk_fma_f32 v[4:5], v[100:101], v[182:183], v[4:5]
	v_pk_mul_f32 v[8:9], v[14:15], v[8:9] op_sel_hi:[0,1]
	v_pk_mul_f32 v[4:5], v[14:15], v[4:5] op_sel_hi:[0,1]
	v_med3_f32 v12, v116, s56, v212
	v_med3_f32 v13, v117, s56, v212
	v_med3_f32 v6, v8, s56, v212
	v_med3_f32 v7, v9, s56, v212
	v_med3_f32 v2, v4, s56, v212
	v_med3_f32 v3, v5, s56, v212
	v_cvt_pk_fp8_f32 v125, v12, v13 op_sel:[0,0,1]
	v_or_b32_e32 v12, v15, v191
	v_cvt_pk_fp8_f32 v107, v17, v19 op_sel:[0,0,1]
	v_cvt_pk_fp8_f32 v108, v6, v7 op_sel:[0,0,1]
	v_cvt_pk_fp8_f32 v109, v2, v3 op_sel:[0,0,1]
	v_or_b32_e32 v2, v15, v192
	v_ashrrev_i32_e32 v11, 31, v10
	v_ashrrev_i32_e32 v13, 31, v12
	v_ashrrev_i32_e32 v3, 31, v2
	v_lshlrev_b64 v[10:11], 10, v[10:11]
	v_lshlrev_b64 v[12:13], 10, v[12:13]
	v_lshlrev_b64 v[2:3], 10, v[2:3]
	v_lshl_add_u64 v[10:11], s[92:93], 0, v[10:11]
	v_lshl_add_u64 v[12:13], s[92:93], 0, v[12:13]
	v_lshl_add_u64 v[2:3], s[92:93], 0, v[2:3]
	v_permlane16_swap_b32_e32 v138, v140
	v_permlane16_swap_b32_e32 v139, v141
	v_lshl_add_u64 v[10:11], v[10:11], 0, v[30:31]
	v_permlane16_swap_b32_e32 v122, v124
	v_permlane16_swap_b32_e32 v123, v125
	v_lshl_add_u64 v[12:13], v[12:13], 0, v[30:31]
	v_permlane16_swap_b32_e32 v106, v108
	v_permlane16_swap_b32_e32 v107, v109
	v_lshl_add_u64 v[30:31], v[2:3], 0, v[30:31]
	global_store_dwordx4 v[10:11], v[138:141], off
	global_store_dwordx4 v[12:13], v[122:125], off
	global_store_dwordx4 v[30:31], v[106:109], off
	global_load_dwordx4 v[2:5], v[180:181], off offset:528
	global_load_dwordx4 v[6:9], v[180:181], off offset:512
	s_nop 0
	global_load_dwordx4 v[104:107], v[32:33], off offset:528
	global_load_dwordx4 v[98:101], v[32:33], off offset:512
	s_waitcnt vmcnt(1)
	v_pk_mul_f32 v[32:33], v[106:107], s[8:9] op_sel_hi:[1,0]
	s_waitcnt vmcnt(0)
	v_pk_mul_f32 v[102:103], v[98:99], s[8:9] op_sel_hi:[1,0]
	v_pk_mul_f32 v[98:99], v[104:105], s[8:9] op_sel_hi:[1,0]
	v_pk_fma_f32 v[94:95], v[94:95], v[102:103], v[6:7]
	v_pk_fma_f32 v[90:91], v[90:91], v[98:99], v[2:3]
	v_pk_mul_f32 v[94:95], v[28:29], v[94:95] op_sel_hi:[0,1]
	v_pk_mul_f32 v[104:105], v[28:29], v[90:91] op_sel_hi:[0,1]
	v_med3_f32 v15, v94, s56, v212
	v_med3_f32 v17, v95, s56, v212
	s_nop 0
	v_pk_mul_f32 v[100:101], v[100:101], s[8:9] op_sel_hi:[1,0]
	v_cvt_pk_fp8_f32 v90, v15, v17
	v_pk_fma_f32 v[96:97], v[96:97], v[100:101], v[8:9]
	s_nop 0
	v_pk_mul_f32 v[96:97], v[28:29], v[96:97] op_sel_hi:[0,1]
	v_med3_f32 v15, v96, s56, v212
	v_med3_f32 v17, v97, s56, v212
	v_cvt_pk_fp8_f32 v90, v15, v17 op_sel:[0,0,1]
	v_med3_f32 v15, v104, s56, v212
	v_med3_f32 v17, v105, s56, v212
	v_cvt_pk_fp8_f32 v91, v15, v17
	v_pk_fma_f32 v[92:93], v[92:93], v[32:33], v[4:5]
	v_pk_fma_f32 v[86:87], v[86:87], v[102:103], v[6:7]
	v_pk_mul_f32 v[28:29], v[28:29], v[92:93] op_sel_hi:[0,1]
	v_med3_f32 v15, v28, s56, v212
	v_med3_f32 v17, v29, s56, v212
	v_pk_mul_f32 v[86:87], v[26:27], v[86:87] op_sel_hi:[0,1]
	v_cvt_pk_fp8_f32 v91, v15, v17 op_sel:[0,0,1]
	v_med3_f32 v15, v86, s56, v212
	v_med3_f32 v17, v87, s56, v212
	s_nop 0
	v_cvt_pk_fp8_f32 v92, v15, v17
	v_pk_fma_f32 v[28:29], v[88:89], v[100:101], v[8:9]
	v_pk_fma_f32 v[82:83], v[82:83], v[98:99], v[2:3]
	v_pk_mul_f32 v[28:29], v[26:27], v[28:29] op_sel_hi:[0,1]
	v_pk_mul_f32 v[82:83], v[26:27], v[82:83] op_sel_hi:[0,1]
	v_med3_f32 v15, v28, s56, v212
	v_med3_f32 v17, v29, s56, v212
	v_cvt_pk_fp8_f32 v92, v15, v17 op_sel:[0,0,1]
	v_med3_f32 v15, v82, s56, v212
	v_med3_f32 v17, v83, s56, v212
	s_nop 0
	v_cvt_pk_fp8_f32 v93, v15, v17
	v_pk_fma_f32 v[84:85], v[84:85], v[32:33], v[4:5]
	v_pk_fma_f32 v[28:29], v[78:79], v[102:103], v[6:7]
	v_pk_mul_f32 v[26:27], v[26:27], v[84:85] op_sel_hi:[0,1]
	v_med3_f32 v15, v26, s56, v212
	v_med3_f32 v17, v27, s56, v212
	v_pk_fma_f32 v[26:27], v[80:81], v[100:101], v[8:9]
	v_pk_mul_f32 v[28:29], v[24:25], v[28:29] op_sel_hi:[0,1]
	v_pk_fma_f32 v[76:77], v[76:77], v[32:33], v[4:5]
	v_pk_fma_f32 v[74:75], v[74:75], v[98:99], v[2:3]
	v_cvt_pk_fp8_f32 v93, v15, v17 op_sel:[0,0,1]
	v_pk_mul_f32 v[26:27], v[24:25], v[26:27] op_sel_hi:[0,1]
	v_pk_mul_f32 v[74:75], v[24:25], v[74:75] op_sel_hi:[0,1]
	v_pk_mul_f32 v[76:77], v[24:25], v[76:77] op_sel_hi:[0,1]
	v_med3_f32 v15, v28, s56, v212
	v_med3_f32 v17, v29, s56, v212
	s_nop 0
	v_cvt_pk_fp8_f32 v24, v15, v17
	v_med3_f32 v15, v26, s56, v212
	v_med3_f32 v17, v27, s56, v212
	s_nop 0
	v_cvt_pk_fp8_f32 v24, v15, v17 op_sel:[0,0,1]
	v_med3_f32 v15, v74, s56, v212
	v_med3_f32 v17, v75, s56, v212
	v_cvt_pk_fp8_f32 v25, v15, v17
	v_pk_fma_f32 v[26:27], v[64:65], v[100:101], v[8:9]
	v_pk_fma_f32 v[28:29], v[62:63], v[102:103], v[6:7]
	v_med3_f32 v15, v76, s56, v212
	v_med3_f32 v17, v77, s56, v212
	v_pk_mul_f32 v[28:29], v[22:23], v[28:29] op_sel_hi:[0,1]
	v_pk_mul_f32 v[62:63], v[22:23], v[26:27] op_sel_hi:[0,1]
	v_pk_fma_f32 v[26:27], v[60:61], v[32:33], v[4:5]
	v_pk_fma_f32 v[58:59], v[58:59], v[98:99], v[2:3]
	v_cvt_pk_fp8_f32 v25, v15, v17 op_sel:[0,0,1]
	v_pk_mul_f32 v[58:59], v[22:23], v[58:59] op_sel_hi:[0,1]
	v_pk_mul_f32 v[22:23], v[22:23], v[26:27] op_sel_hi:[0,1]
	v_med3_f32 v15, v28, s56, v212
	v_med3_f32 v17, v29, s56, v212
	s_nop 0
	v_cvt_pk_fp8_f32 v26, v15, v17
	v_med3_f32 v15, v62, s56, v212
	v_med3_f32 v17, v63, s56, v212
	s_nop 0
	v_cvt_pk_fp8_f32 v26, v15, v17 op_sel:[0,0,1]
	v_med3_f32 v15, v58, s56, v212
	v_med3_f32 v17, v59, s56, v212
	v_cvt_pk_fp8_f32 v27, v15, v17
	v_med3_f32 v15, v22, s56, v212
	v_med3_f32 v17, v23, s56, v212
	v_permlane16_swap_b32_e32 v24, v26
	v_cvt_pk_fp8_f32 v27, v15, v17 op_sel:[0,0,1]
	v_pk_fma_f32 v[22:23], v[70:71], v[102:103], v[6:7]
	v_permlane16_swap_b32_e32 v90, v92
	v_permlane16_swap_b32_e32 v25, v27
	global_store_dwordx4 v[10:11], v[24:27], off offset:128
	v_pk_fma_f32 v[10:11], v[72:73], v[100:101], v[8:9]
	v_pk_mul_f32 v[22:23], v[20:21], v[22:23] op_sel_hi:[0,1]
	v_pk_fma_f32 v[24:25], v[68:69], v[32:33], v[4:5]
	v_pk_fma_f32 v[26:27], v[66:67], v[98:99], v[2:3]
	v_pk_mul_f32 v[10:11], v[20:21], v[10:11] op_sel_hi:[0,1]
	v_pk_mul_f32 v[26:27], v[20:21], v[26:27] op_sel_hi:[0,1]
	v_pk_mul_f32 v[24:25], v[20:21], v[24:25] op_sel_hi:[0,1]
	v_med3_f32 v15, v22, s56, v212
	v_med3_f32 v17, v23, s56, v212
	s_nop 0
	v_cvt_pk_fp8_f32 v20, v15, v17
	v_med3_f32 v10, v10, s56, v212
	v_med3_f32 v11, v11, s56, v212
	s_nop 0
	v_cvt_pk_fp8_f32 v20, v10, v11 op_sel:[0,0,1]
	v_med3_f32 v10, v26, s56, v212
	v_med3_f32 v11, v27, s56, v212
	v_cvt_pk_fp8_f32 v21, v10, v11
	v_pk_fma_f32 v[22:23], v[54:55], v[102:103], v[6:7]
	v_med3_f32 v10, v24, s56, v212
	v_pk_mul_f32 v[22:23], v[18:19], v[22:23] op_sel_hi:[0,1]
	v_med3_f32 v15, v22, s56, v212
	v_med3_f32 v17, v23, s56, v212
	s_nop 0
	v_med3_f32 v11, v25, s56, v212
	v_cvt_pk_fp8_f32 v22, v15, v17
	v_cvt_pk_fp8_f32 v21, v10, v11 op_sel:[0,0,1]
	v_pk_fma_f32 v[10:11], v[56:57], v[100:101], v[8:9]
	v_pk_fma_f32 v[26:27], v[50:51], v[98:99], v[2:3]
	v_pk_mul_f32 v[10:11], v[18:19], v[10:11] op_sel_hi:[0,1]
	v_pk_mul_f32 v[26:27], v[18:19], v[26:27] op_sel_hi:[0,1]
	v_med3_f32 v10, v10, s56, v212
	v_med3_f32 v11, v11, s56, v212
	v_cvt_pk_fp8_f32 v22, v10, v11 op_sel:[0,0,1]
	v_med3_f32 v10, v26, s56, v212
	v_med3_f32 v11, v27, s56, v212
	s_nop 0
	v_cvt_pk_fp8_f32 v23, v10, v11
	v_pk_fma_f32 v[24:25], v[52:53], v[32:33], v[4:5]
	v_permlane16_swap_b32_e32 v20, v22
	v_pk_mul_f32 v[18:19], v[18:19], v[24:25] op_sel_hi:[0,1]
	v_med3_f32 v10, v18, s56, v212
	v_med3_f32 v11, v19, s56, v212
	v_cvt_pk_fp8_f32 v23, v10, v11 op_sel:[0,0,1]
	v_pk_fma_f32 v[10:11], v[48:49], v[100:101], v[8:9]
	v_pk_fma_f32 v[8:9], v[40:41], v[100:101], v[8:9]
	v_pk_mul_f32 v[18:19], v[16:17], v[10:11] op_sel_hi:[0,1]
	v_permlane16_swap_b32_e32 v21, v23
	global_store_dwordx4 v[12:13], v[20:23], off offset:128
	v_pk_fma_f32 v[12:13], v[46:47], v[102:103], v[6:7]
	v_pk_fma_f32 v[10:11], v[44:45], v[32:33], v[4:5]
	v_pk_mul_f32 v[12:13], v[16:17], v[12:13] op_sel_hi:[0,1]
	v_pk_fma_f32 v[20:21], v[42:43], v[98:99], v[2:3]
	v_pk_fma_f32 v[6:7], v[38:39], v[102:103], v[6:7]
	v_pk_mul_f32 v[20:21], v[16:17], v[20:21] op_sel_hi:[0,1]
	v_pk_mul_f32 v[16:17], v[16:17], v[10:11] op_sel_hi:[0,1]
	v_med3_f32 v11, v12, s56, v212
	v_med3_f32 v12, v13, s56, v212
	s_nop 0
	v_cvt_pk_fp8_f32 v10, v11, v12
	v_med3_f32 v11, v18, s56, v212
	v_med3_f32 v12, v19, s56, v212
	v_med3_f32 v13, v21, s56, v212
	v_cvt_pk_fp8_f32 v10, v11, v12 op_sel:[0,0,1]
	v_med3_f32 v12, v20, s56, v212
	s_nop 0
	v_cvt_pk_fp8_f32 v11, v12, v13
	v_pk_fma_f32 v[2:3], v[34:35], v[98:99], v[2:3]
	v_med3_f32 v12, v16, s56, v212
	v_med3_f32 v13, v17, s56, v212
	v_pk_mul_f32 v[6:7], v[14:15], v[6:7] op_sel_hi:[0,1]
	v_pk_mul_f32 v[2:3], v[14:15], v[2:3] op_sel_hi:[0,1]
	v_cvt_pk_fp8_f32 v11, v12, v13 op_sel:[0,0,1]
	v_med3_f32 v6, v6, s56, v212
	v_med3_f32 v7, v7, s56, v212
	s_nop 0
	v_med3_f32 v2, v2, s56, v212
	v_med3_f32 v3, v3, s56, v212
	s_nop 0
	v_cvt_pk_fp8_f32 v12, v6, v7
	v_cvt_pk_fp8_f32 v13, v2, v3
	v_pk_fma_f32 v[4:5], v[36:37], v[32:33], v[4:5]
	v_pk_mul_f32 v[8:9], v[14:15], v[8:9] op_sel_hi:[0,1]
	v_pk_mul_f32 v[4:5], v[14:15], v[4:5] op_sel_hi:[0,1]
	v_med3_f32 v6, v8, s56, v212
	v_med3_f32 v7, v9, s56, v212
	v_med3_f32 v2, v4, s56, v212
	v_med3_f32 v3, v5, s56, v212
	v_cvt_pk_fp8_f32 v12, v6, v7 op_sel:[0,0,1]
	v_cvt_pk_fp8_f32 v13, v2, v3 op_sel:[0,0,1]
	v_permlane16_swap_b32_e32 v91, v93
	v_permlane16_swap_b32_e32 v10, v12
	v_permlane16_swap_b32_e32 v11, v13
	global_store_dwordx4 v[146:147], v[90:93], off offset:128
	global_store_dwordx4 v[30:31], v[10:13], off offset:128
	s_cbranch_vccnz .LBB0_581
	s_andn2_b64 vcc, exec, s[2:3]
	s_cbranch_vccnz .LBB0_580
	s_barrier
	s_branch .LBB0_580

.LBB0_2751:
	v_add_u32_e32 v179, s39, v151
	v_add_u32_e32 v225, v179, v155
	v_add_u32_e32 v224, v179, v181
	v_add_u32_e32 v223, v179, v219
	s_waitcnt lgkmcnt(0)
	v_lshrrev_b32_e32 v82, v163, v226
	v_bfe_i32 v83, v82, 26, 1
	v_bitop3_b32 v96, v16, s28, v83 bitop3:0xe4
	v_bfe_i32 v83, v82, 25, 1
	v_bitop3_b32 v95, v13, s28, v83 bitop3:0xe4
	v_bfe_i32 v83, v82, 24, 1
	v_bitop3_b32 v94, v14, s28, v83 bitop3:0xe4
	v_bfe_i32 v83, v82, 19, 1
	v_bitop3_b32 v93, v11, s28, v83 bitop3:0xe4
	v_bfe_i32 v83, v82, 18, 1
	v_bitop3_b32 v92, v12, s28, v83 bitop3:0xe4
	v_bfe_i32 v83, v82, 17, 1
	v_add_u32_e32 v226, v179, v153
	v_bitop3_b32 v91, v9, s28, v83 bitop3:0xe4
	v_bfe_i32 v83, v82, 16, 1
	ds_read_b128 v[186:189], v226
	v_bitop3_b32 v90, v10, s28, v83 bitop3:0xe4
	v_bfe_i32 v83, v82, 11, 1
	v_bitop3_b32 v89, v7, s28, v83 bitop3:0xe4
	v_bfe_i32 v83, v82, 10, 1
	v_bitop3_b32 v88, v8, s28, v83 bitop3:0xe4
	v_bfe_i32 v83, v82, 9, 1
	v_bitop3_b32 v87, v5, s28, v83 bitop3:0xe4
	v_bfe_i32 v83, v82, 8, 1
	v_bitop3_b32 v86, v6, s28, v83 bitop3:0xe4
	v_bfe_i32 v83, v82, 3, 1
	v_bfe_i32 v84, v82, 27, 1
	v_bitop3_b32 v85, v3, s28, v83 bitop3:0xe4
	v_bfe_i32 v83, v82, 2, 1
	v_bitop3_b32 v97, v15, s28, v84 bitop3:0xe4
	v_bitop3_b32 v84, v4, s28, v83 bitop3:0xe4
	v_bfe_i32 v83, v82, 1, 1
	v_bfe_i32 v82, v82, 0, 1
	v_bitop3_b32 v83, v1, s28, v83 bitop3:0xe4
	v_bitop3_b32 v82, v2, s28, v82 bitop3:0xe4
	v_add_u32_e32 v179, s39, v17
	s_add_i32 s14, s37, 1
	s_waitcnt lgkmcnt(0)
	v_mfma_f32_32x32x16_bf16 v[98:113], v[186:189], v[114:117], v[82:97]
	s_cmp_lg_u32 s37, 2
	s_cselect_b32 s37, s14, 0
	s_add_u32 s0, s0, 0x4000
	s_addc_u32 s1, s1, 0
	s_add_i32 s38, s38, 1
	s_cmp_eq_u32 s36, s0
	v_add_u32_e32 v146, 8, v146
	v_mfma_f32_32x32x16_bf16 v[82:97], v[186:189], v[130:133], v[82:97]
	ds_read_b128 v[186:189], v225
	s_waitcnt lgkmcnt(0)
	v_mfma_f32_32x32x16_bf16 v[98:113], v[186:189], v[118:121], v[98:113]
	v_mfma_f32_32x32x16_bf16 v[82:97], v[186:189], v[134:137], v[82:97]
	ds_read_b128 v[186:189], v224
	s_waitcnt lgkmcnt(0)
	v_mfma_f32_32x32x16_bf16 v[98:113], v[186:189], v[122:125], v[98:113]
	v_mfma_f32_32x32x16_bf16 v[82:97], v[186:189], v[138:141], v[82:97]
	ds_read_b128 v[186:189], v223
	s_waitcnt lgkmcnt(0)
	v_mfma_f32_32x32x16_bf16 v[98:113], v[186:189], v[126:129], v[98:113]
	v_mfma_f32_32x32x16_bf16 v[82:97], v[186:189], v[142:145], v[82:97]
	s_nop 10
	v_exp_f32_e32 v190, v98
	v_exp_f32_e32 v191, v99
	v_exp_f32_e32 v192, v100
	v_exp_f32_e32 v193, v101
	s_nop 0
	ds_read_b64_tr_b16 v[98:99], v179 offset:49152
	ds_read_b64_tr_b16 v[100:101], v179 offset:50176
	v_exp_f32_e32 v188, v102
	v_exp_f32_e32 v189, v103
	v_exp_f32_e32 v186, v104
	v_exp_f32_e32 v187, v105
	ds_read_b64_tr_b16 v[212:213], v179 offset:50688
	ds_read_b64_tr_b16 v[210:211], v179 offset:49664
	v_exp_f32_e32 v204, v82
	v_exp_f32_e32 v205, v83
	v_exp_f32_e32 v208, v84
	v_exp_f32_e32 v209, v85
	v_exp_f32_e32 v200, v86
	v_exp_f32_e32 v201, v87
	v_exp_f32_e32 v196, v88
	v_exp_f32_e32 v197, v89
	v_cvt_pk_bf16_f32 v102, v190, v191
	v_cvt_pk_bf16_f32 v103, v192, v193
	v_cvt_pk_bf16_f32 v104, v188, v189
	v_cvt_pk_bf16_f32 v105, v186, v187
	v_cvt_pk_bf16_f32 v82, v204, v205
	v_cvt_pk_bf16_f32 v83, v208, v209
	s_waitcnt lgkmcnt(2)
	v_mfma_f32_32x32x16_bf16 v[66:81], v[98:101], v[102:105], v[66:81]
	v_cvt_pk_bf16_f32 v84, v200, v201
	v_cvt_pk_bf16_f32 v85, v196, v197
	v_exp_f32_e32 v206, v106
	v_exp_f32_e32 v207, v107
	v_exp_f32_e32 v202, v108
	v_exp_f32_e32 v203, v109
	v_exp_f32_e32 v198, v110
	s_waitcnt lgkmcnt(0)
	v_mfma_f32_32x32x16_bf16 v[50:65], v[210:213], v[102:105], v[50:65]
	v_exp_f32_e32 v199, v111
	v_exp_f32_e32 v194, v112
	v_exp_f32_e32 v195, v113
	v_exp_f32_e32 v216, v90
	v_exp_f32_e32 v217, v91
	v_exp_f32_e32 v214, v92
	v_exp_f32_e32 v215, v93
	v_mfma_f32_32x32x16_bf16 v[34:49], v[98:101], v[82:85], v[34:49]
	v_cvt_pk_bf16_f32 v86, v206, v207
	v_cvt_pk_bf16_f32 v87, v202, v203
	v_cvt_pk_bf16_f32 v88, v198, v199
	v_cvt_pk_bf16_f32 v89, v194, v195
	v_mfma_f32_32x32x16_bf16 v[18:33], v[210:213], v[82:85], v[18:33]
	ds_read_b64_tr_b16 v[82:83], v179 offset:51200
	ds_read_b64_tr_b16 v[84:85], v179 offset:52224
	ds_read_b64_tr_b16 v[100:101], v179 offset:52736
	ds_read_b64_tr_b16 v[98:99], v179 offset:51712
	v_exp_f32_e32 v212, v94
	v_exp_f32_e32 v213, v95
	v_exp_f32_e32 v210, v96
	v_exp_f32_e32 v211, v97
	s_waitcnt lgkmcnt(2)
	v_mfma_f32_32x32x16_bf16 v[66:81], v[82:85], v[86:89], v[66:81]
	s_waitcnt lgkmcnt(0)
	v_mfma_f32_32x32x16_bf16 v[50:65], v[98:101], v[86:89], v[50:65]
	v_cvt_pk_bf16_f32 v86, v216, v217
	v_cvt_pk_bf16_f32 v87, v214, v215
	v_cvt_pk_bf16_f32 v88, v212, v213
	v_cvt_pk_bf16_f32 v89, v210, v211
	s_nop 1
	v_mfma_f32_32x32x16_bf16 v[34:49], v[82:85], v[86:89], v[34:49]
	v_lshrrev_b32_e32 v82, v163, v227
	v_bfe_i32 v83, v82, 26, 1
	v_bitop3_b32 v96, v16, s28, v83 bitop3:0xe4
	v_bfe_i32 v83, v82, 25, 1
	v_bitop3_b32 v95, v13, s28, v83 bitop3:0xe4
	v_bfe_i32 v83, v82, 24, 1
	v_bitop3_b32 v94, v14, s28, v83 bitop3:0xe4
	v_bfe_i32 v83, v82, 19, 1
	v_bitop3_b32 v93, v11, s28, v83 bitop3:0xe4
	v_bfe_i32 v83, v82, 18, 1
	v_bitop3_b32 v92, v12, s28, v83 bitop3:0xe4
	v_bfe_i32 v83, v82, 17, 1
	v_bitop3_b32 v91, v9, s28, v83 bitop3:0xe4
	v_bfe_i32 v83, v82, 16, 1
	ds_read_b128 v[226:229], v226 offset:4096
	v_bitop3_b32 v90, v10, s28, v83 bitop3:0xe4
	v_bfe_i32 v83, v82, 11, 1
	v_mfma_f32_32x32x16_bf16 v[18:33], v[98:101], v[86:89], v[18:33]
	v_bitop3_b32 v89, v7, s28, v83 bitop3:0xe4
	v_bfe_i32 v83, v82, 10, 1
	v_bitop3_b32 v88, v8, s28, v83 bitop3:0xe4
	v_bfe_i32 v83, v82, 9, 1
	v_bitop3_b32 v87, v5, s28, v83 bitop3:0xe4
	v_bfe_i32 v83, v82, 8, 1
	v_bitop3_b32 v86, v6, s28, v83 bitop3:0xe4
	v_bfe_i32 v83, v82, 3, 1
	v_bfe_i32 v84, v82, 27, 1
	v_bitop3_b32 v85, v3, s28, v83 bitop3:0xe4
	v_bfe_i32 v83, v82, 2, 1
	v_bitop3_b32 v97, v15, s28, v84 bitop3:0xe4
	v_bitop3_b32 v84, v4, s28, v83 bitop3:0xe4
	v_bfe_i32 v83, v82, 1, 1
	v_bfe_i32 v82, v82, 0, 1
	v_bitop3_b32 v83, v1, s28, v83 bitop3:0xe4
	v_bitop3_b32 v82, v2, s28, v82 bitop3:0xe4
	s_waitcnt lgkmcnt(0)
	s_nop 0
	v_mfma_f32_32x32x16_bf16 v[98:113], v[226:229], v[114:117], v[82:97]
	v_mfma_f32_32x32x16_bf16 v[82:97], v[226:229], v[130:133], v[82:97]
	ds_read_b128 v[226:229], v225 offset:4096
	s_waitcnt lgkmcnt(0)
	v_mfma_f32_32x32x16_bf16 v[98:113], v[226:229], v[118:121], v[98:113]
	v_mfma_f32_32x32x16_bf16 v[82:97], v[226:229], v[134:137], v[82:97]
	ds_read_b128 v[224:227], v224 offset:4096
	s_waitcnt lgkmcnt(0)
	v_mfma_f32_32x32x16_bf16 v[98:113], v[224:227], v[122:125], v[98:113]
	v_mfma_f32_32x32x16_bf16 v[82:97], v[224:227], v[138:141], v[82:97]
	ds_read_b128 v[224:227], v223 offset:4096
	s_waitcnt lgkmcnt(0)
	v_mfma_f32_32x32x16_bf16 v[98:113], v[224:227], v[126:129], v[98:113]
	v_mfma_f32_32x32x16_bf16 v[82:97], v[224:227], v[142:145], v[82:97]
	s_nop 10
	v_exp_f32_e32 v228, v98
	v_exp_f32_e32 v229, v99
	v_exp_f32_e32 v230, v100
	v_exp_f32_e32 v231, v101
	ds_read_b64_tr_b16 v[98:99], v179 offset:53248
	ds_read_b64_tr_b16 v[100:101], v179 offset:54272
	v_exp_f32_e32 v232, v102
	v_exp_f32_e32 v233, v103
	v_exp_f32_e32 v234, v104
	v_exp_f32_e32 v235, v105
	ds_read_b64_tr_b16 v[226:227], v179 offset:54784
	ds_read_b64_tr_b16 v[224:225], v179 offset:53760
	v_cvt_pk_bf16_f32 v102, v228, v229
	v_cvt_pk_bf16_f32 v103, v230, v231
	v_cvt_pk_bf16_f32 v104, v232, v233
	v_cvt_pk_bf16_f32 v105, v234, v235
	v_exp_f32_e32 v236, v86
	v_exp_f32_e32 v237, v87
	s_waitcnt lgkmcnt(2)
	v_mfma_f32_32x32x16_bf16 v[66:81], v[98:101], v[102:105], v[66:81]
	v_exp_f32_e32 v238, v88
	v_exp_f32_e32 v239, v89
	v_exp_f32_e32 v106, v106
	v_exp_f32_e32 v107, v107
	v_exp_f32_e32 v108, v108
	v_exp_f32_e32 v109, v109
	v_exp_f32_e32 v110, v110
	s_waitcnt lgkmcnt(0)
	v_mfma_f32_32x32x16_bf16 v[50:65], v[224:227], v[102:105], v[50:65]
	v_exp_f32_e32 v102, v82
	v_exp_f32_e32 v103, v83
	v_exp_f32_e32 v104, v84
	v_exp_f32_e32 v105, v85
	v_cvt_pk_bf16_f32 v84, v236, v237
	v_cvt_pk_bf16_f32 v82, v102, v103
	v_cvt_pk_bf16_f32 v85, v238, v239
	v_cvt_pk_bf16_f32 v83, v104, v105
	v_exp_f32_e32 v111, v111
	v_exp_f32_e32 v112, v112
	v_mfma_f32_32x32x16_bf16 v[34:49], v[98:101], v[82:85], v[34:49]
	v_exp_f32_e32 v113, v113
	v_exp_f32_e32 v90, v90
	v_exp_f32_e32 v91, v91
	v_exp_f32_e32 v92, v92
	v_exp_f32_e32 v93, v93
	v_exp_f32_e32 v94, v94
	v_exp_f32_e32 v95, v95
	v_mfma_f32_32x32x16_bf16 v[18:33], v[224:227], v[82:85], v[18:33]
	ds_read_b64_tr_b16 v[82:83], v179 offset:55296
	ds_read_b64_tr_b16 v[84:85], v179 offset:56320
	ds_read_b64_tr_b16 v[100:101], v179 offset:56832
	ds_read_b64_tr_b16 v[98:99], v179 offset:55808
	v_exp_f32_e32 v96, v96
	v_exp_f32_e32 v97, v97
	v_cvt_pk_bf16_f32 v86, v106, v107
	v_cvt_pk_bf16_f32 v87, v108, v109
	v_cvt_pk_bf16_f32 v88, v110, v111
	v_cvt_pk_bf16_f32 v89, v112, v113
	s_waitcnt lgkmcnt(2)
	s_nop 0
	v_mfma_f32_32x32x16_bf16 v[66:81], v[82:85], v[86:89], v[66:81]
	s_waitcnt lgkmcnt(0)
	v_mfma_f32_32x32x16_bf16 v[50:65], v[98:101], v[86:89], v[50:65]
	v_cvt_pk_bf16_f32 v86, v90, v91
	v_cvt_pk_bf16_f32 v87, v92, v93
	v_cvt_pk_bf16_f32 v88, v94, v95
	v_cvt_pk_bf16_f32 v89, v96, v97
	s_nop 1
	v_mfma_f32_32x32x16_bf16 v[34:49], v[82:85], v[86:89], v[34:49]
	v_add_f32_e64 v82, v190, 0
	v_add_f32_e64 v83, v191, 0
	v_add_f32_e64 v84, v228, 0
	v_add_f32_e64 v85, v229, 0
	v_add_f32_e64 v82, v192, v82
	v_add_f32_e64 v83, v193, v83
	v_pk_add_f32 v[84:85], v[230:231], v[84:85]
	v_pk_add_f32 v[82:83], v[188:189], v[82:83]
	v_pk_add_f32 v[84:85], v[232:233], v[84:85]
	v_pk_add_f32 v[82:83], v[186:187], v[82:83]
	v_mfma_f32_32x32x16_bf16 v[18:33], v[98:101], v[86:89], v[18:33]
	v_add_f32_e64 v86, v204, 0
	v_add_f32_e64 v87, v205, 0
	v_add_f32_e64 v88, v102, 0
	v_add_f32_e64 v89, v103, 0
	v_add_f32_e64 v86, v208, v86
	v_add_f32_e64 v87, v209, v87
	v_pk_add_f32 v[88:89], v[104:105], v[88:89]
	v_pk_add_f32 v[86:87], v[200:201], v[86:87]
	v_pk_add_f32 v[88:89], v[236:237], v[88:89]
	v_pk_add_f32 v[84:85], v[234:235], v[84:85]
	v_pk_add_f32 v[86:87], v[196:197], v[86:87]
	v_pk_add_f32 v[88:89], v[238:239], v[88:89]
	v_pk_add_f32 v[82:83], v[206:207], v[82:83]
	v_pk_add_f32 v[84:85], v[106:107], v[84:85]
	v_pk_add_f32 v[86:87], v[216:217], v[86:87]
	v_pk_add_f32 v[88:89], v[90:91], v[88:89]
	v_pk_add_f32 v[82:83], v[202:203], v[82:83]
	v_pk_add_f32 v[84:85], v[108:109], v[84:85]
	v_pk_add_f32 v[86:87], v[214:215], v[86:87]
	v_pk_add_f32 v[88:89], v[92:93], v[88:89]
	v_pk_add_f32 v[82:83], v[198:199], v[82:83]
	v_pk_add_f32 v[84:85], v[110:111], v[84:85]
	v_pk_add_f32 v[86:87], v[212:213], v[86:87]
	v_pk_add_f32 v[88:89], v[94:95], v[88:89]
	v_pk_add_f32 v[82:83], v[194:195], v[82:83]
	v_pk_add_f32 v[84:85], v[112:113], v[84:85]
	v_pk_add_f32 v[86:87], v[210:211], v[86:87]
	v_pk_add_f32 v[88:89], v[96:97], v[88:89]
	v_pk_add_f32 v[82:83], v[82:83], v[84:85]
	v_pk_add_f32 v[84:85], v[86:87], v[88:89]
	v_mov_b32_e32 v86, v82
	v_mov_b32_e32 v87, v84
	v_mov_b32_e32 v84, v83
	v_pk_add_f32 v[82:83], v[86:87], v[84:85]
	s_nop 0
	v_pk_add_f32 v[184:185], v[184:185], v[82:83]
	s_cbranch_scc1 .LBB0_2745

.LBB0_2756:
	s_barrier
	ds_read_b64 v[226:227], v146
	s_cmp_le_u32 s38, s34
	s_mov_b64 s[14:15], -1
	s_cbranch_scc0 .LBB0_2758
	s_lshl_b32 s39, s37, 14
	s_add_i32 s14, s39, 0xffffc000
	s_cmp_lg_u32 s37, 0
	s_cselect_b32 s40, s14, 0x8000
	v_lshl_add_u64 v[82:83], v[182:183], 0, s[0:1]
	s_mov_b64 s[14:15], 0x39208000
	s_add_i32 s40, s22, s40
	v_lshl_add_u64 v[84:85], v[82:83], 0, s[14:15]
	s_mov_b32 m0, s40
	s_mov_b64 s[14:15], 0x39208080
	global_load_lds_dwordx4 v[84:85], off
	v_lshl_add_u64 v[82:83], v[82:83], 0, s[14:15]
	s_add_i32 m0, s40, 0x2000
	s_mov_b64 s[14:15], 0x3a208000
	global_load_lds_dwordx4 v[82:83], off
	v_lshl_add_u64 v[82:83], v[172:173], 0, s[0:1]
	v_lshl_add_u64 v[84:85], v[82:83], 0, s[14:15]
	s_add_i32 m0, s40, 0xc000
	v_lshl_add_u64 v[82:83], v[82:83], 0, s[12:13]
	global_load_lds_dwordx4 v[84:85], off
	s_add_i32 m0, s40, 0xe000
	s_mov_b64 s[14:15], 0
	global_load_lds_dwordx4 v[82:83], off

.LBB0_3083:
	s_lshl_b32 s1, s26, 2
	s_add_i32 s1, s1, 0
	s_add_i32 s1, s1, 0x20480
	v_mov_b32_e32 v74, s1
	s_ashr_i32 s27, s26, 31
	ds_read_b32 v74, v74
	s_lshl_b64 s[22:23], s[26:27], 13
	s_add_u32 s28, s47, s22
	s_addc_u32 s29, s48, s23
	s_add_u32 s1, s45, s22
	s_addc_u32 s19, s46, s23
	s_lshl_b32 s22, s24, 8
	v_lshl_or_b32 v201, s24, 7, v170
	s_waitcnt lgkmcnt(0)
	v_sub_u32_e32 v74, s57, v74
	s_ashr_i32 s23, s22, 31
	v_lshl_add_u32 v172, v74, 8, v178
	v_lshlrev_b32_e32 v74, 1, v201
	s_lshl_b64 s[22:23], s[22:23], 2
	v_ashrrev_i32_e32 v75, 31, v74
	s_add_u32 s22, s1, s22
	v_lshl_add_u64 v[82:83], v[74:75], 2, s[28:29]
	s_addc_u32 s23, s19, s23
	v_lshlrev_b32_e32 v110, 2, v170
	global_load_dwordx4 v[98:101], v[82:83], off offset:16
	global_load_dwordx4 v[114:117], v[82:83], off
	global_load_dwordx4 v[74:77], v[82:83], off offset:48
	global_load_dwordx4 v[90:93], v[82:83], off offset:32
	s_nop 0
	global_load_dwordx4 v[82:85], v110, s[22:23] offset:16
	global_load_dwordx4 v[106:109], v110, s[22:23]
	global_load_dwordx4 v[86:89], v110, s[22:23] offset:528
	s_nop 0
	global_load_dwordx4 v[110:113], v110, s[22:23] offset:512
	s_lshl_b64 s[22:23], s[26:27], 18
	s_add_u32 s22, s66, s22
	v_ashrrev_i32_e32 v173, 31, v172
	s_addc_u32 s23, s67, s23
	v_lshl_add_u64 v[172:173], v[172:173], 2, s[22:23]
	global_load_dword v200, v[172:173], off
	global_load_dword v206, v[172:173], off offset:64
	v_cvt_f32_i32_e32 v161, v161
	v_cvt_f32_i32_e32 v160, v160
	v_cvt_f32_i32_e32 v159, v159
	v_cvt_f32_i32_e32 v158, v158
	v_cvt_f32_i32_e32 v202, v150
	v_cvt_f32_i32_e32 v203, v151
	v_cvt_f32_i32_e32 v153, v153
	v_cvt_f32_i32_e32 v152, v152
	v_cvt_f32_i32_e32 v157, v157
	v_cvt_f32_i32_e32 v156, v156
	v_cvt_f32_i32_e32 v155, v155
	v_cvt_f32_i32_e32 v154, v154
	v_cvt_f32_i32_e32 v205, v147
	v_cvt_f32_i32_e32 v204, v146
	v_cvt_f32_i32_e32 v149, v149
	v_cvt_f32_i32_e32 v148, v148
	v_cvt_f32_i32_e32 v143, v143
	v_cvt_f32_i32_e32 v142, v142
	v_cvt_f32_i32_e32 v139, v139
	v_cvt_f32_i32_e32 v138, v138
	v_cvt_f32_i32_e32 v135, v135
	v_cvt_f32_i32_e32 v134, v134
	v_cvt_f32_i32_e32 v141, v141
	v_cvt_f32_i32_e32 v140, v140
	v_cvt_f32_i32_e32 v131, v131
	v_cvt_f32_i32_e32 v130, v130
	v_cvt_f32_i32_e32 v137, v137
	v_cvt_f32_i32_e32 v136, v136
	v_cvt_f32_i32_e32 v133, v133
	v_cvt_f32_i32_e32 v132, v132
	v_lshl_add_u32 v169, s57, 8, v178
	v_sub_u32_e32 v146, v201, v179
	v_ashrrev_i32_e32 v147, 31, v146
	v_cvt_f32_i32_e32 v127, v127
	v_cvt_f32_i32_e32 v126, v126
	v_cvt_f32_i32_e32 v129, v129
	v_cvt_f32_i32_e32 v128, v128
	v_cvt_f32_i32_e32 v123, v123
	v_cvt_f32_i32_e32 v122, v122
	v_cvt_f32_i32_e32 v125, v125
	v_cvt_f32_i32_e32 v124, v124
	v_cvt_f32_i32_e32 v119, v119
	v_cvt_f32_i32_e32 v118, v118
	v_cvt_f32_i32_e32 v121, v121
	v_cvt_f32_i32_e32 v120, v120
	v_cvt_f32_i32_e32 v103, v103
	v_cvt_f32_i32_e32 v102, v102
	v_cvt_f32_i32_e32 v105, v105
	v_cvt_f32_i32_e32 v104, v104
	v_cvt_f32_i32_e32 v95, v95
	v_cvt_f32_i32_e32 v94, v94
	v_cvt_f32_i32_e32 v79, v79
	v_cvt_f32_i32_e32 v78, v78
	v_cvt_f32_i32_e32 v97, v97
	v_cvt_f32_i32_e32 v96, v96
	v_cvt_f32_i32_e32 v71, v71
	v_cvt_f32_i32_e32 v70, v70
	v_cvt_f32_i32_e32 v81, v81
	v_cvt_f32_i32_e32 v80, v80
	v_cvt_f32_i32_e32 v67, v67
	v_cvt_f32_i32_e32 v66, v66
	v_cvt_f32_i32_e32 v73, v73
	v_cvt_f32_i32_e32 v72, v72
	v_cvt_f32_i32_e32 v69, v69
	v_cvt_f32_i32_e32 v68, v68
	v_cvt_f32_i32_e32 v65, v65
	v_cvt_f32_i32_e32 v64, v64
	v_cvt_f32_i32_e32 v59, v59
	s_waitcnt vmcnt(0)
	v_mov_b32_e32 v150, v99
	v_mov_b32_e32 v99, v100
	v_pk_mul_f32 v[160:161], v[108:109], v[160:161]
	v_mov_b32_e32 v210, v75
	v_mov_b32_e32 v211, v77
	v_mov_b32_e32 v212, v91
	v_mov_b32_e32 v213, v93
	v_mov_b32_e32 v91, v92
	v_pk_add_f32 v[92:93], v[210:211], 1.0 op_sel_hi:[1,0]
	v_mov_b32_e32 v208, v115
	v_pk_fma_f32 v[160:161], v[160:161], v[200:201], v[98:99] op_sel_hi:[1,0,1]
	v_mov_b32_e32 v115, v116
	v_min_f32_e32 v160, 0x40e00000, v160
	v_min_f32_e32 v161, 0x40e00000, v161
	v_pk_mul_f32 v[210:211], v[160:161], s[12:13] op_sel_hi:[1,0]
	v_pk_mul_f32 v[158:159], v[106:107], v[158:159]
	v_exp_f32_e32 v210, v210
	v_exp_f32_e32 v211, v211
	v_pk_fma_f32 v[158:159], v[158:159], v[200:201], v[114:115] op_sel_hi:[1,0,1]
	v_mov_b32_e32 v151, v101
	v_mov_b32_e32 v209, v117
	v_pk_mul_f32 v[202:203], v[82:83], v[202:203]
	v_min_f32_e32 v158, 0x40e00000, v158
	v_min_f32_e32 v159, 0x40e00000, v159
	v_mov_b32_e32 v75, v76
	v_pk_mul_f32 v[76:77], v[84:85], v[152:153]
	v_pk_add_f32 v[116:117], v[150:151], 1.0 op_sel_hi:[1,0]
	v_pk_add_f32 v[150:151], v[208:209], 1.0 op_sel_hi:[1,0]
	v_pk_fma_f32 v[202:203], v[202:203], v[200:201], v[90:91] op_sel_hi:[1,0,1]
	v_pk_mul_f32 v[208:209], v[158:159], s[12:13] op_sel_hi:[1,0]
	v_pk_fma_f32 v[76:77], v[76:77], v[200:201], v[74:75] op_sel_hi:[1,0,1]
	v_min_f32_e32 v202, 0x40e00000, v202
	v_exp_f32_e32 v208, v208
	v_exp_f32_e32 v209, v209
	v_min_f32_e32 v203, 0x40e00000, v203
	v_pk_fma_f32 v[210:211], v[210:211], s[14:15], s[14:15] op_sel_hi:[1,0,0]
	v_min_f32_e32 v76, 0x40e00000, v76
	v_min_f32_e32 v77, 0x40e00000, v77
	v_pk_add_f32 v[100:101], v[212:213], 1.0 op_sel_hi:[1,0]
	v_pk_mul_f32 v[212:213], v[202:203], s[12:13] op_sel_hi:[1,0]
	v_rcp_f32_e32 v210, v210
	v_rcp_f32_e32 v211, v211
	v_pk_mul_f32 v[152:153], v[76:77], s[12:13] op_sel_hi:[1,0]
	v_exp_f32_e32 v212, v212
	v_exp_f32_e32 v213, v213
	v_exp_f32_e32 v152, v152
	v_exp_f32_e32 v153, v153
	v_pk_mul_f32 v[156:157], v[112:113], v[156:157]
	v_pk_fma_f32 v[208:209], v[208:209], s[14:15], s[14:15] op_sel_hi:[1,0,0]
	v_pk_fma_f32 v[156:157], v[156:157], v[200:201], v[116:117] op_sel_hi:[1,0,1]
	v_rcp_f32_e32 v208, v208
	v_med3_f32 v156, v156, s55, v199
	v_med3_f32 v157, v157, s55, v199
	v_rcp_f32_e32 v209, v209
	v_pk_mul_f32 v[160:161], v[160:161], v[210:211]
	v_pk_fma_f32 v[152:153], v[152:153], s[14:15], s[14:15] op_sel_hi:[1,0,0]
	v_pk_mul_f32 v[156:157], v[156:157], v[160:161]
	v_pk_fma_f32 v[160:161], v[212:213], s[14:15], s[14:15] op_sel_hi:[1,0,0]
	v_pk_mul_f32 v[154:155], v[110:111], v[154:155]
	v_rcp_f32_e32 v160, v160
	v_rcp_f32_e32 v161, v161
	v_rcp_f32_e32 v152, v152
	v_rcp_f32_e32 v153, v153
	v_pk_fma_f32 v[154:155], v[154:155], v[200:201], v[150:151] op_sel_hi:[1,0,1]
	v_pk_mul_f32 v[204:205], v[86:87], v[204:205]
	v_med3_f32 v154, v154, s55, v199
	v_med3_f32 v155, v155, s55, v199
	v_pk_mul_f32 v[158:159], v[158:159], v[208:209]
	v_pk_mul_f32 v[148:149], v[88:89], v[148:149]
	v_pk_mul_f32 v[142:143], v[106:107], v[142:143]
	v_pk_mul_f32 v[154:155], v[154:155], v[158:159]
	v_pk_fma_f32 v[158:159], v[204:205], v[200:201], v[100:101] op_sel_hi:[1,0,1]
	v_pk_fma_f32 v[148:149], v[148:149], v[200:201], v[92:93] op_sel_hi:[1,0,1]
	v_pk_fma_f32 v[142:143], v[142:143], v[206:207], v[114:115] op_sel_hi:[1,0,1]
	v_med3_f32 v158, v158, s55, v199
	v_med3_f32 v159, v159, s55, v199
	v_pk_mul_f32 v[160:161], v[202:203], v[160:161]
	v_med3_f32 v148, v148, s55, v199
	v_med3_f32 v149, v149, s55, v199
	v_pk_mul_f32 v[76:77], v[76:77], v[152:153]
	v_min_f32_e32 v142, 0x40e00000, v142
	v_min_f32_e32 v143, 0x40e00000, v143
	v_pk_mul_f32 v[158:159], v[158:159], v[160:161]
	v_pk_mul_f32 v[76:77], v[148:149], v[76:77]
	s_nop 0
	v_pk_mul_f32 v[148:149], v[142:143], s[12:13] op_sel_hi:[1,0]
	v_cvt_pk_fp8_f32 v153, v158, v159
	v_exp_f32_e32 v148, v148
	v_exp_f32_e32 v149, v149
	v_pk_mul_f32 v[134:135], v[82:83], v[134:135]
	v_cvt_pk_fp8_f32 v153, v76, v77 op_sel:[0,0,1]
	v_pk_mul_f32 v[76:77], v[110:111], v[138:139]
	v_pk_fma_f32 v[138:139], v[148:149], s[14:15], s[14:15] op_sel_hi:[1,0,0]
	v_pk_fma_f32 v[76:77], v[76:77], v[206:207], v[150:151] op_sel_hi:[1,0,1]
	v_rcp_f32_e32 v138, v138
	v_rcp_f32_e32 v139, v139
	v_med3_f32 v76, v76, s55, v199
	v_med3_f32 v77, v77, s55, v199
	v_pk_fma_f32 v[134:135], v[134:135], v[206:207], v[90:91] op_sel_hi:[1,0,1]
	v_pk_mul_f32 v[138:139], v[142:143], v[138:139]
	v_cvt_f32_i32_e32 v143, v145
	v_cvt_f32_i32_e32 v142, v144
	v_pk_mul_f32 v[76:77], v[76:77], v[138:139]
	v_min_f32_e32 v134, 0x40e00000, v134
	v_min_f32_e32 v135, 0x40e00000, v135
	v_pk_mul_f32 v[138:139], v[108:109], v[142:143]
	v_pk_mul_f32 v[144:145], v[134:135], s[12:13] op_sel_hi:[1,0]
	v_pk_fma_f32 v[138:139], v[138:139], v[206:207], v[98:99] op_sel_hi:[1,0,1]
	v_exp_f32_e32 v144, v144
	v_min_f32_e32 v138, 0x40e00000, v138
	v_min_f32_e32 v139, 0x40e00000, v139
	v_pk_mul_f32 v[142:143], v[138:139], s[12:13] op_sel_hi:[1,0]
	v_exp_f32_e32 v145, v145
	v_exp_f32_e32 v142, v142
	v_exp_f32_e32 v143, v143
	v_pk_mul_f32 v[140:141], v[112:113], v[140:141]
	v_pk_mul_f32 v[130:131], v[86:87], v[130:131]
	v_pk_fma_f32 v[140:141], v[140:141], v[206:207], v[116:117] op_sel_hi:[1,0,1]
	v_pk_fma_f32 v[142:143], v[142:143], s[14:15], s[14:15] op_sel_hi:[1,0,0]
	v_med3_f32 v140, v140, s55, v199
	v_rcp_f32_e32 v142, v142
	v_rcp_f32_e32 v143, v143
	v_med3_f32 v141, v141, s55, v199
	v_pk_fma_f32 v[130:131], v[130:131], v[206:207], v[100:101] op_sel_hi:[1,0,1]
	s_nop 0
	v_pk_mul_f32 v[138:139], v[138:139], v[142:143]
	v_med3_f32 v130, v130, s55, v199
	v_pk_mul_f32 v[138:139], v[140:141], v[138:139]
	v_pk_fma_f32 v[140:141], v[144:145], s[14:15], s[14:15] op_sel_hi:[1,0,0]
	v_med3_f32 v131, v131, s55, v199
	v_rcp_f32_e32 v140, v140
	v_rcp_f32_e32 v141, v141
	v_cvt_pk_fp8_f32 v152, v154, v155
	s_nop 0
	s_nop 0
	v_pk_mul_f32 v[134:135], v[134:135], v[140:141]
	v_pk_mul_f32 v[132:133], v[88:89], v[132:133]
	v_pk_mul_f32 v[130:131], v[130:131], v[134:135]
	v_pk_mul_f32 v[134:135], v[84:85], v[136:137]
	v_cvt_pk_fp8_f32 v154, v76, v77
	v_pk_fma_f32 v[134:135], v[134:135], v[206:207], v[74:75] op_sel_hi:[1,0,1]
	v_cvt_pk_fp8_f32 v155, v130, v131
	v_min_f32_e32 v134, 0x40e00000, v134
	v_min_f32_e32 v135, 0x40e00000, v135
	v_pk_mul_f32 v[136:137], v[134:135], s[12:13] op_sel_hi:[1,0]
	v_pk_fma_f32 v[132:133], v[132:133], v[206:207], v[92:93] op_sel_hi:[1,0,1]
	v_exp_f32_e32 v136, v136
	v_exp_f32_e32 v137, v137
	v_med3_f32 v132, v132, s55, v199
	v_med3_f32 v133, v133, s55, v199
	v_cvt_pk_fp8_f32 v152, v156, v157 op_sel:[0,0,1]
	v_pk_fma_f32 v[136:137], v[136:137], s[14:15], s[14:15] op_sel_hi:[1,0,0]
	v_cvt_pk_fp8_f32 v154, v138, v139 op_sel:[0,0,1]
	v_rcp_f32_e32 v136, v136
	v_rcp_f32_e32 v137, v137
	v_pk_mul_f32 v[126:127], v[106:107], v[126:127]
	v_permlane16_swap_b32_e32 v152, v154
	v_pk_mul_f32 v[76:77], v[134:135], v[136:137]
	v_pk_mul_f32 v[128:129], v[108:109], v[128:129]
	v_pk_mul_f32 v[76:77], v[132:133], v[76:77]
	v_pk_mul_f32 v[122:123], v[110:111], v[122:123]
	v_cvt_pk_fp8_f32 v155, v76, v77 op_sel:[0,0,1]
	v_or_b32_e32 v76, v169, v180
	v_ashrrev_i32_e32 v77, 31, v76
	v_lshlrev_b64 v[76:77], 10, v[76:77]
	v_lshl_add_u64 v[76:77], s[94:95], 0, v[76:77]
	v_permlane16_swap_b32_e32 v153, v155
	v_lshl_add_u64 v[76:77], v[76:77], 0, v[146:147]
	global_store_dwordx4 v[76:77], v[152:155], off
	global_load_dword v76, v[172:173], off offset:128
	v_pk_mul_f32 v[124:125], v[112:113], v[124:125]
	global_load_dword v130, v[172:173], off offset:192
	v_pk_mul_f32 v[118:119], v[82:83], v[118:119]
	v_pk_mul_f32 v[120:121], v[84:85], v[120:121]
	v_pk_mul_f32 v[102:103], v[86:87], v[102:103]
	v_pk_mul_f32 v[104:105], v[88:89], v[104:105]
	v_pk_mul_f32 v[94:95], v[106:107], v[94:95]
	v_pk_mul_f32 v[78:79], v[110:111], v[78:79]
	v_pk_mul_f32 v[70:71], v[82:83], v[70:71]
	v_pk_mul_f32 v[80:81], v[112:113], v[80:81]
	v_pk_mul_f32 v[66:67], v[86:87], v[66:67]
	v_pk_mul_f32 v[68:69], v[88:89], v[68:69]
	v_pk_mul_f32 v[64:65], v[108:109], v[64:65]
	v_cvt_f32_i32_e32 v58, v58
	v_cvt_f32_i32_e32 v61, v61
	v_cvt_f32_i32_e32 v60, v60
	v_cvt_f32_i32_e32 v55, v55
	v_pk_mul_f32 v[58:59], v[110:111], v[58:59]
	v_cvt_f32_i32_e32 v54, v54
	v_pk_mul_f32 v[60:61], v[112:113], v[60:61]
	v_cvt_f32_i32_e32 v57, v57
	v_cvt_f32_i32_e32 v56, v56
	v_pk_mul_f32 v[54:55], v[82:83], v[54:55]
	v_cvt_f32_i32_e32 v51, v51
	v_cvt_f32_i32_e32 v50, v50
	v_pk_mul_f32 v[56:57], v[84:85], v[56:57]
	v_cvt_f32_i32_e32 v53, v53
	v_cvt_f32_i32_e32 v52, v52
	v_pk_mul_f32 v[50:51], v[86:87], v[50:51]
	v_cvt_f32_i32_e32 v47, v47
	v_cvt_f32_i32_e32 v46, v46
	v_cvt_f32_i32_e32 v43, v43
	v_cvt_f32_i32_e32 v42, v42
	v_cvt_f32_i32_e32 v49, v49
	v_pk_mul_f32 v[46:47], v[106:107], v[46:47]
	v_cvt_f32_i32_e32 v48, v48
	v_pk_mul_f32 v[42:43], v[110:111], v[42:43]
	v_cvt_f32_i32_e32 v39, v39
	v_cvt_f32_i32_e32 v38, v38
	v_cvt_f32_i32_e32 v45, v45
	v_cvt_f32_i32_e32 v44, v44
	v_cvt_f32_i32_e32 v31, v31
	v_pk_mul_f32 v[38:39], v[82:83], v[38:39]
	v_cvt_f32_i32_e32 v30, v30
	v_pk_mul_f32 v[44:45], v[112:113], v[44:45]
	v_cvt_f32_i32_e32 v41, v41
	v_cvt_f32_i32_e32 v40, v40
	v_pk_mul_f32 v[30:31], v[86:87], v[30:31]
	v_cvt_f32_i32_e32 v33, v33
	v_cvt_f32_i32_e32 v32, v32
	v_cvt_f32_i32_e32 v23, v23
	v_cvt_f32_i32_e32 v22, v22
	v_cvt_f32_i32_e32 v25, v25
	v_pk_mul_f32 v[32:33], v[88:89], v[32:33]
	v_cvt_f32_i32_e32 v24, v24
	v_pk_mul_f32 v[22:23], v[106:107], v[22:23]
	v_cvt_f32_i32_e32 v37, v37
	v_cvt_f32_i32_e32 v36, v36
	v_pk_mul_f32 v[24:25], v[108:109], v[24:25]
	v_cvt_f32_i32_e32 v15, v15
	v_cvt_f32_i32_e32 v14, v14
	v_cvt_f32_i32_e32 v17, v17
	v_cvt_f32_i32_e32 v16, v16
	v_cvt_f32_i32_e32 v27, v27
	v_pk_mul_f32 v[14:15], v[82:83], v[14:15]
	v_cvt_f32_i32_e32 v26, v26
	v_pk_mul_f32 v[16:17], v[84:85], v[16:17]
	v_cvt_f32_i32_e32 v29, v29
	v_cvt_f32_i32_e32 v28, v28
	v_pk_mul_f32 v[26:27], v[86:87], v[26:27]
	v_cvt_f32_i32_e32 v7, v7
	v_cvt_f32_i32_e32 v6, v6
	v_cvt_f32_i32_e32 v19, v19
	v_cvt_f32_i32_e32 v18, v18
	v_cvt_f32_i32_e32 v9, v9
	v_pk_mul_f32 v[6:7], v[106:107], v[6:7]
	v_cvt_f32_i32_e32 v8, v8
	v_cvt_f32_i32_e32 v3, v3
	v_cvt_f32_i32_e32 v2, v2
	s_waitcnt vmcnt(1)
	v_pk_fma_f32 v[126:127], v[126:127], v[76:77], v[114:115] op_sel_hi:[1,0,1]
	v_pk_fma_f32 v[128:129], v[128:129], v[76:77], v[98:99] op_sel_hi:[1,0,1]
	v_min_f32_e32 v126, 0x40e00000, v126
	v_min_f32_e32 v127, 0x40e00000, v127
	v_pk_mul_f32 v[132:133], v[126:127], s[12:13] op_sel_hi:[1,0]
	v_min_f32_e32 v128, 0x40e00000, v128
	v_exp_f32_e32 v132, v132
	v_exp_f32_e32 v133, v133
	v_min_f32_e32 v129, 0x40e00000, v129
	v_pk_mul_f32 v[134:135], v[128:129], s[12:13] op_sel_hi:[1,0]
	v_pk_fma_f32 v[122:123], v[122:123], v[76:77], v[150:151] op_sel_hi:[1,0,1]
	v_pk_fma_f32 v[132:133], v[132:133], s[14:15], s[14:15] op_sel_hi:[1,0,0]
	v_exp_f32_e32 v134, v134
	v_rcp_f32_e32 v132, v132
	v_rcp_f32_e32 v133, v133
	v_exp_f32_e32 v135, v135
	v_med3_f32 v122, v122, s55, v199
	v_med3_f32 v123, v123, s55, v199
	v_pk_mul_f32 v[126:127], v[126:127], v[132:133]
	v_pk_fma_f32 v[124:125], v[124:125], v[76:77], v[116:117] op_sel_hi:[1,0,1]
	v_pk_mul_f32 v[122:123], v[122:123], v[126:127]
	v_pk_fma_f32 v[126:127], v[134:135], s[14:15], s[14:15] op_sel_hi:[1,0,0]
	v_pk_fma_f32 v[118:119], v[118:119], v[76:77], v[90:91] op_sel_hi:[1,0,1]
	v_rcp_f32_e32 v126, v126
	v_rcp_f32_e32 v127, v127
	v_med3_f32 v124, v124, s55, v199
	v_med3_f32 v125, v125, s55, v199
	v_min_f32_e32 v118, 0x40e00000, v118
	v_pk_mul_f32 v[126:127], v[128:129], v[126:127]
	v_min_f32_e32 v119, 0x40e00000, v119
	v_pk_mul_f32 v[124:125], v[124:125], v[126:127]
	v_pk_mul_f32 v[126:127], v[118:119], s[12:13] op_sel_hi:[1,0]
	v_pk_fma_f32 v[120:121], v[120:121], v[76:77], v[74:75] op_sel_hi:[1,0,1]
	v_exp_f32_e32 v126, v126
	v_exp_f32_e32 v127, v127
	v_min_f32_e32 v120, 0x40e00000, v120
	v_min_f32_e32 v121, 0x40e00000, v121
	v_pk_mul_f32 v[128:129], v[120:121], s[12:13] op_sel_hi:[1,0]
	v_pk_fma_f32 v[126:127], v[126:127], s[14:15], s[14:15] op_sel_hi:[1,0,0]
	v_exp_f32_e32 v128, v128
	v_rcp_f32_e32 v126, v126
	v_rcp_f32_e32 v127, v127
	v_exp_f32_e32 v129, v129
	v_pk_fma_f32 v[102:103], v[102:103], v[76:77], v[100:101] op_sel_hi:[1,0,1]
	v_pk_fma_f32 v[76:77], v[104:105], v[76:77], v[92:93] op_sel_hi:[1,0,1]
	v_med3_f32 v102, v102, s55, v199
	v_med3_f32 v103, v103, s55, v199
	v_pk_mul_f32 v[118:119], v[118:119], v[126:127]
	v_med3_f32 v76, v76, s55, v199
	v_pk_mul_f32 v[102:103], v[102:103], v[118:119]
	v_pk_fma_f32 v[118:119], v[128:129], s[14:15], s[14:15] op_sel_hi:[1,0,0]
	v_med3_f32 v77, v77, s55, v199
	v_rcp_f32_e32 v118, v118
	v_rcp_f32_e32 v119, v119
	s_waitcnt vmcnt(0)
	v_pk_fma_f32 v[94:95], v[94:95], v[130:131], v[114:115] op_sel_hi:[1,0,1]
	v_pk_fma_f32 v[78:79], v[78:79], v[130:131], v[150:151] op_sel_hi:[1,0,1]
	v_min_f32_e32 v94, 0x40e00000, v94
	v_pk_mul_f32 v[104:105], v[120:121], v[118:119]
	v_min_f32_e32 v95, 0x40e00000, v95
	v_pk_mul_f32 v[104:105], v[76:77], v[104:105]
	s_nop 0
	v_cvt_pk_fp8_f32 v77, v102, v103
	v_pk_mul_f32 v[102:103], v[94:95], s[12:13] op_sel_hi:[1,0]
	v_med3_f32 v78, v78, s55, v199
	v_exp_f32_e32 v102, v102
	v_exp_f32_e32 v103, v103
	v_med3_f32 v79, v79, s55, v199
	v_pk_fma_f32 v[70:71], v[70:71], v[130:131], v[90:91] op_sel_hi:[1,0,1]
	v_pk_fma_f32 v[80:81], v[80:81], v[130:131], v[116:117] op_sel_hi:[1,0,1]
	v_pk_fma_f32 v[102:103], v[102:103], s[14:15], s[14:15] op_sel_hi:[1,0,0]
	v_min_f32_e32 v70, 0x40e00000, v70
	v_rcp_f32_e32 v102, v102
	v_rcp_f32_e32 v103, v103
	v_min_f32_e32 v71, 0x40e00000, v71
	v_med3_f32 v80, v80, s55, v199
	v_med3_f32 v81, v81, s55, v199
	v_pk_mul_f32 v[94:95], v[94:95], v[102:103]
	v_pk_mul_f32 v[102:103], v[70:71], s[12:13] op_sel_hi:[1,0]
	v_pk_mul_f32 v[94:95], v[78:79], v[94:95]
	v_pk_mul_f32 v[78:79], v[108:109], v[96:97]
	v_exp_f32_e32 v102, v102
	v_pk_fma_f32 v[78:79], v[78:79], v[130:131], v[98:99] op_sel_hi:[1,0,1]
	v_exp_f32_e32 v103, v103
	v_min_f32_e32 v78, 0x40e00000, v78
	v_min_f32_e32 v79, 0x40e00000, v79
	v_pk_mul_f32 v[96:97], v[78:79], s[12:13] op_sel_hi:[1,0]
	v_pk_fma_f32 v[66:67], v[66:67], v[130:131], v[100:101] op_sel_hi:[1,0,1]
	v_exp_f32_e32 v96, v96
	v_exp_f32_e32 v97, v97
	v_med3_f32 v66, v66, s55, v199
	v_med3_f32 v67, v67, s55, v199
	s_nop 0
	v_pk_fma_f32 v[96:97], v[96:97], s[14:15], s[14:15] op_sel_hi:[1,0,0]
	v_cvt_pk_fp8_f32 v76, v122, v123
	v_rcp_f32_e32 v96, v96
	v_rcp_f32_e32 v97, v97
	v_pk_fma_f32 v[68:69], v[68:69], v[130:131], v[92:93] op_sel_hi:[1,0,1]
	v_cvt_pk_fp8_f32 v76, v124, v125 op_sel:[0,0,1]
	v_med3_f32 v68, v68, s55, v199
	v_pk_mul_f32 v[78:79], v[78:79], v[96:97]
	v_med3_f32 v69, v69, s55, v199
	v_pk_mul_f32 v[80:81], v[80:81], v[78:79]
	v_pk_fma_f32 v[78:79], v[102:103], s[14:15], s[14:15] op_sel_hi:[1,0,0]
	v_cvt_pk_fp8_f32 v77, v104, v105 op_sel:[0,0,1]
	v_rcp_f32_e32 v78, v78
	v_rcp_f32_e32 v79, v79
	v_pk_mul_f32 v[8:9], v[108:109], v[8:9]
	v_pk_mul_f32 v[2:3], v[82:83], v[2:3]
	v_cvt_f32_i32_e32 v11, v11
	v_pk_mul_f32 v[70:71], v[70:71], v[78:79]
	s_nop 0
	v_pk_mul_f32 v[66:67], v[66:67], v[70:71]
	v_pk_mul_f32 v[70:71], v[84:85], v[72:73]
	s_nop 0
	v_pk_fma_f32 v[70:71], v[70:71], v[130:131], v[74:75] op_sel_hi:[1,0,1]
	v_cvt_pk_fp8_f32 v78, v94, v95
	v_min_f32_e32 v70, 0x40e00000, v70
	v_min_f32_e32 v71, 0x40e00000, v71
	v_pk_mul_f32 v[72:73], v[70:71], s[12:13] op_sel_hi:[1,0]
	v_cvt_pk_fp8_f32 v79, v66, v67
	v_exp_f32_e32 v72, v72
	v_exp_f32_e32 v73, v73
	v_cvt_pk_fp8_f32 v78, v80, v81 op_sel:[0,0,1]
	v_cvt_f32_i32_e32 v10, v10
	v_cvt_f32_i32_e32 v5, v5
	v_pk_fma_f32 v[72:73], v[72:73], s[14:15], s[14:15] op_sel_hi:[1,0,0]
	v_permlane16_swap_b32_e32 v76, v78
	v_rcp_f32_e32 v72, v72
	v_rcp_f32_e32 v73, v73
	v_cvt_f32_i32_e32 v4, v4
	v_cvt_f32_i32_e32 v13, v13
	v_cvt_f32_i32_e32 v12, v12
	v_pk_mul_f32 v[66:67], v[70:71], v[72:73]
	v_pk_mul_f32 v[10:11], v[86:87], v[10:11]
	v_pk_mul_f32 v[66:67], v[68:69], v[66:67]
	v_cvt_f32_i32_e32 v69, v63
	v_cvt_pk_fp8_f32 v79, v66, v67 op_sel:[0,0,1]
	v_or_b32_e32 v66, v169, v181
	v_ashrrev_i32_e32 v67, 31, v66
	v_lshlrev_b64 v[66:67], 10, v[66:67]
	v_lshl_add_u64 v[66:67], s[94:95], 0, v[66:67]
	v_permlane16_swap_b32_e32 v77, v79
	v_lshl_add_u64 v[66:67], v[66:67], 0, v[146:147]
	global_store_dwordx4 v[66:67], v[76:79], off
	global_load_dword v66, v[172:173], off offset:512
	v_cvt_f32_i32_e32 v68, v62
	global_load_dword v70, v[172:173], off offset:576
	v_add_u32_e32 v62, 0x80, v169
	v_pk_mul_f32 v[4:5], v[84:85], v[4:5]
	v_pk_mul_f32 v[68:69], v[106:107], v[68:69]
	s_and_b64 vcc, exec, s[2:3]
	s_mov_b64 s[2:3], -1
	s_mov_b32 s59, s62
	s_mov_b32 s58, s63
	s_waitcnt vmcnt(1)
	v_pk_fma_f32 v[68:69], v[68:69], v[66:67], v[114:115] op_sel_hi:[1,0,1]
	s_nop 0
	v_min_f32_e32 v68, 0x40e00000, v68
	v_min_f32_e32 v69, 0x40e00000, v69
	v_pk_mul_f32 v[72:73], v[68:69], s[12:13] op_sel_hi:[1,0]
	v_pk_fma_f32 v[64:65], v[64:65], v[66:67], v[98:99] op_sel_hi:[1,0,1]
	v_exp_f32_e32 v72, v72
	v_exp_f32_e32 v73, v73
	v_min_f32_e32 v64, 0x40e00000, v64
	v_min_f32_e32 v65, 0x40e00000, v65
	v_pk_mul_f32 v[76:77], v[64:65], s[12:13] op_sel_hi:[1,0]
	v_pk_fma_f32 v[72:73], v[72:73], s[14:15], s[14:15] op_sel_hi:[1,0,0]
	v_exp_f32_e32 v76, v76
	v_rcp_f32_e32 v72, v72
	v_rcp_f32_e32 v73, v73
	v_exp_f32_e32 v77, v77
	v_pk_fma_f32 v[58:59], v[58:59], v[66:67], v[150:151] op_sel_hi:[1,0,1]
	v_pk_fma_f32 v[60:61], v[60:61], v[66:67], v[116:117] op_sel_hi:[1,0,1]
	v_med3_f32 v58, v58, s55, v199
	v_med3_f32 v59, v59, s55, v199
	v_pk_mul_f32 v[68:69], v[68:69], v[72:73]
	v_pk_fma_f32 v[54:55], v[54:55], v[66:67], v[90:91] op_sel_hi:[1,0,1]
	v_pk_mul_f32 v[58:59], v[58:59], v[68:69]
	v_pk_fma_f32 v[68:69], v[76:77], s[14:15], s[14:15] op_sel_hi:[1,0,0]
	v_med3_f32 v60, v60, s55, v199
	v_rcp_f32_e32 v68, v68
	v_rcp_f32_e32 v69, v69
	v_med3_f32 v61, v61, s55, v199
	v_min_f32_e32 v54, 0x40e00000, v54
	v_min_f32_e32 v55, 0x40e00000, v55
	v_pk_mul_f32 v[64:65], v[64:65], v[68:69]
	v_pk_fma_f32 v[56:57], v[56:57], v[66:67], v[74:75] op_sel_hi:[1,0,1]
	v_pk_mul_f32 v[60:61], v[60:61], v[64:65]
	v_pk_mul_f32 v[64:65], v[54:55], s[12:13] op_sel_hi:[1,0]
	v_min_f32_e32 v56, 0x40e00000, v56
	v_exp_f32_e32 v64, v64
	v_exp_f32_e32 v65, v65
	v_min_f32_e32 v57, 0x40e00000, v57
	v_pk_mul_f32 v[68:69], v[56:57], s[12:13] op_sel_hi:[1,0]
	v_pk_fma_f32 v[50:51], v[50:51], v[66:67], v[100:101] op_sel_hi:[1,0,1]
	v_pk_fma_f32 v[64:65], v[64:65], s[14:15], s[14:15] op_sel_hi:[1,0,0]
	v_exp_f32_e32 v68, v68
	v_rcp_f32_e32 v64, v64
	v_rcp_f32_e32 v65, v65
	v_exp_f32_e32 v69, v69
	v_med3_f32 v50, v50, s55, v199
	v_med3_f32 v51, v51, s55, v199
	v_pk_mul_f32 v[54:55], v[54:55], v[64:65]
	s_waitcnt vmcnt(0)
	v_pk_fma_f32 v[46:47], v[46:47], v[70:71], v[114:115] op_sel_hi:[1,0,1]
	v_pk_mul_f32 v[54:55], v[50:51], v[54:55]
	v_pk_mul_f32 v[50:51], v[88:89], v[52:53]
	v_pk_fma_f32 v[52:53], v[68:69], s[14:15], s[14:15] op_sel_hi:[1,0,0]
	v_pk_fma_f32 v[50:51], v[50:51], v[66:67], v[92:93] op_sel_hi:[1,0,1]
	v_rcp_f32_e32 v52, v52
	v_rcp_f32_e32 v53, v53
	v_med3_f32 v50, v50, s55, v199
	v_med3_f32 v51, v51, s55, v199
	v_min_f32_e32 v46, 0x40e00000, v46
	v_pk_mul_f32 v[52:53], v[56:57], v[52:53]
	v_min_f32_e32 v47, 0x40e00000, v47
	v_pk_mul_f32 v[52:53], v[50:51], v[52:53]
	s_nop 0
	v_cvt_pk_fp8_f32 v51, v54, v55
	v_pk_mul_f32 v[54:55], v[46:47], s[12:13] op_sel_hi:[1,0]
	v_pk_fma_f32 v[42:43], v[42:43], v[70:71], v[150:151] op_sel_hi:[1,0,1]
	v_exp_f32_e32 v54, v54
	v_exp_f32_e32 v55, v55
	v_cvt_pk_fp8_f32 v51, v52, v53 op_sel:[0,0,1]
	v_med3_f32 v42, v42, s55, v199
	v_med3_f32 v43, v43, s55, v199
	v_pk_fma_f32 v[52:53], v[54:55], s[14:15], s[14:15] op_sel_hi:[1,0,0]
	v_pk_fma_f32 v[38:39], v[38:39], v[70:71], v[90:91] op_sel_hi:[1,0,1]
	v_rcp_f32_e32 v52, v52
	v_rcp_f32_e32 v53, v53
	v_min_f32_e32 v38, 0x40e00000, v38
	v_min_f32_e32 v39, 0x40e00000, v39
	v_pk_fma_f32 v[44:45], v[44:45], v[70:71], v[116:117] op_sel_hi:[1,0,1]
	v_pk_mul_f32 v[46:47], v[46:47], v[52:53]
	v_pk_mul_f32 v[52:53], v[38:39], s[12:13] op_sel_hi:[1,0]
	v_pk_mul_f32 v[42:43], v[42:43], v[46:47]
	v_pk_mul_f32 v[46:47], v[108:109], v[48:49]
	v_exp_f32_e32 v52, v52
	v_pk_fma_f32 v[46:47], v[46:47], v[70:71], v[98:99] op_sel_hi:[1,0,1]
	v_exp_f32_e32 v53, v53
	v_min_f32_e32 v46, 0x40e00000, v46
	v_min_f32_e32 v47, 0x40e00000, v47
	v_pk_mul_f32 v[48:49], v[46:47], s[12:13] op_sel_hi:[1,0]
	v_med3_f32 v44, v44, s55, v199
	v_exp_f32_e32 v48, v48
	v_exp_f32_e32 v49, v49
	v_med3_f32 v45, v45, s55, v199
	v_pk_fma_f32 v[30:31], v[30:31], v[70:71], v[100:101] op_sel_hi:[1,0,1]
	s_nop 0
	v_pk_fma_f32 v[48:49], v[48:49], s[14:15], s[14:15] op_sel_hi:[1,0,0]
	v_med3_f32 v30, v30, s55, v199
	v_rcp_f32_e32 v48, v48
	v_rcp_f32_e32 v49, v49
	v_med3_f32 v31, v31, s55, v199
	v_cvt_pk_fp8_f32 v50, v58, v59
	v_pk_fma_f32 v[32:33], v[32:33], v[70:71], v[92:93] op_sel_hi:[1,0,1]
	v_pk_mul_f32 v[46:47], v[46:47], v[48:49]
	v_med3_f32 v32, v32, s55, v199
	v_pk_mul_f32 v[44:45], v[44:45], v[46:47]
	v_pk_fma_f32 v[46:47], v[52:53], s[14:15], s[14:15] op_sel_hi:[1,0,0]
	s_nop 0
	v_rcp_f32_e32 v46, v46
	v_rcp_f32_e32 v47, v47
	s_nop 0
	v_cvt_pk_fp8_f32 v52, v42, v43
	v_med3_f32 v33, v33, s55, v199
	v_pk_mul_f32 v[38:39], v[38:39], v[46:47]
	v_cvt_pk_fp8_f32 v50, v60, v61 op_sel:[0,0,1]
	v_pk_mul_f32 v[30:31], v[30:31], v[38:39]
	v_pk_mul_f32 v[38:39], v[84:85], v[40:41]
	v_cvt_pk_fp8_f32 v53, v30, v31
	v_pk_fma_f32 v[38:39], v[38:39], v[70:71], v[74:75] op_sel_hi:[1,0,1]
	v_cvt_pk_fp8_f32 v52, v44, v45 op_sel:[0,0,1]
	v_min_f32_e32 v38, 0x40e00000, v38
	v_min_f32_e32 v39, 0x40e00000, v39
	v_pk_mul_f32 v[40:41], v[38:39], s[12:13] op_sel_hi:[1,0]
	v_permlane16_swap_b32_e32 v50, v52
	v_exp_f32_e32 v40, v40
	v_exp_f32_e32 v41, v41
	s_nop 0
	v_pk_fma_f32 v[40:41], v[40:41], s[14:15], s[14:15] op_sel_hi:[1,0,0]
	s_nop 0
	v_rcp_f32_e32 v40, v40
	v_rcp_f32_e32 v41, v41
	s_nop 0
	v_pk_mul_f32 v[30:31], v[38:39], v[40:41]
	s_nop 0
	v_pk_mul_f32 v[30:31], v[32:33], v[30:31]
	v_cvt_f32_i32_e32 v32, v34
	v_cvt_pk_fp8_f32 v53, v30, v31 op_sel:[0,0,1]
	v_or_b32_e32 v30, v62, v180
	v_ashrrev_i32_e32 v31, 31, v30
	v_lshlrev_b64 v[30:31], 10, v[30:31]
	v_lshl_add_u64 v[30:31], s[94:95], 0, v[30:31]
	v_permlane16_swap_b32_e32 v51, v53
	v_lshl_add_u64 v[30:31], v[30:31], 0, v[146:147]
	global_store_dwordx4 v[30:31], v[50:53], off
	global_load_dword v30, v[172:173], off offset:640
	v_cvt_f32_i32_e32 v33, v35
	global_load_dword v34, v[172:173], off offset:704
	v_pk_mul_f32 v[32:33], v[110:111], v[32:33]
	s_waitcnt vmcnt(1)
	v_pk_fma_f32 v[22:23], v[22:23], v[30:31], v[114:115] op_sel_hi:[1,0,1]
	s_nop 0
	v_min_f32_e32 v22, 0x40e00000, v22
	v_min_f32_e32 v23, 0x40e00000, v23
	v_pk_mul_f32 v[38:39], v[22:23], s[12:13] op_sel_hi:[1,0]
	v_pk_fma_f32 v[24:25], v[24:25], v[30:31], v[98:99] op_sel_hi:[1,0,1]
	v_exp_f32_e32 v38, v38
	v_exp_f32_e32 v39, v39
	v_min_f32_e32 v24, 0x40e00000, v24
	v_min_f32_e32 v25, 0x40e00000, v25
	v_pk_mul_f32 v[40:41], v[24:25], s[12:13] op_sel_hi:[1,0]
	v_pk_fma_f32 v[38:39], v[38:39], s[14:15], s[14:15] op_sel_hi:[1,0,0]
	v_exp_f32_e32 v40, v40
	v_rcp_f32_e32 v38, v38
	v_rcp_f32_e32 v39, v39
	v_exp_f32_e32 v41, v41
	v_pk_fma_f32 v[32:33], v[32:33], v[30:31], v[150:151] op_sel_hi:[1,0,1]
	v_pk_fma_f32 v[14:15], v[14:15], v[30:31], v[90:91] op_sel_hi:[1,0,1]
	v_med3_f32 v32, v32, s55, v199
	v_med3_f32 v33, v33, s55, v199
	v_pk_mul_f32 v[22:23], v[22:23], v[38:39]
	v_min_f32_e32 v14, 0x40e00000, v14
	v_pk_mul_f32 v[22:23], v[32:33], v[22:23]
	v_pk_mul_f32 v[32:33], v[112:113], v[36:37]
	v_pk_fma_f32 v[36:37], v[40:41], s[14:15], s[14:15] op_sel_hi:[1,0,0]
	v_pk_fma_f32 v[32:33], v[32:33], v[30:31], v[116:117] op_sel_hi:[1,0,1]
	v_rcp_f32_e32 v36, v36
	v_rcp_f32_e32 v37, v37
	v_med3_f32 v32, v32, s55, v199
	v_med3_f32 v33, v33, s55, v199
	v_min_f32_e32 v15, 0x40e00000, v15
	v_pk_mul_f32 v[24:25], v[24:25], v[36:37]
	v_pk_fma_f32 v[16:17], v[16:17], v[30:31], v[74:75] op_sel_hi:[1,0,1]
	v_pk_mul_f32 v[24:25], v[32:33], v[24:25]
	v_pk_mul_f32 v[32:33], v[14:15], s[12:13] op_sel_hi:[1,0]
	v_min_f32_e32 v16, 0x40e00000, v16
	v_exp_f32_e32 v32, v32
	v_exp_f32_e32 v33, v33
	v_min_f32_e32 v17, 0x40e00000, v17
	v_pk_mul_f32 v[36:37], v[16:17], s[12:13] op_sel_hi:[1,0]
	v_pk_fma_f32 v[26:27], v[26:27], v[30:31], v[100:101] op_sel_hi:[1,0,1]
	v_pk_fma_f32 v[32:33], v[32:33], s[14:15], s[14:15] op_sel_hi:[1,0,0]
	v_exp_f32_e32 v36, v36
	v_rcp_f32_e32 v32, v32
	v_rcp_f32_e32 v33, v33
	v_exp_f32_e32 v37, v37
	v_med3_f32 v26, v26, s55, v199
	v_med3_f32 v27, v27, s55, v199
	v_pk_mul_f32 v[14:15], v[14:15], v[32:33]
	s_waitcnt vmcnt(0)
	v_pk_fma_f32 v[6:7], v[6:7], v[34:35], v[114:115] op_sel_hi:[1,0,1]
	v_pk_mul_f32 v[26:27], v[26:27], v[14:15]
	v_pk_mul_f32 v[14:15], v[88:89], v[28:29]
	v_pk_fma_f32 v[28:29], v[36:37], s[14:15], s[14:15] op_sel_hi:[1,0,0]
	v_pk_fma_f32 v[14:15], v[14:15], v[30:31], v[92:93] op_sel_hi:[1,0,1]
	v_rcp_f32_e32 v28, v28
	v_rcp_f32_e32 v29, v29
	v_med3_f32 v14, v14, s55, v199
	v_med3_f32 v15, v15, s55, v199
	v_min_f32_e32 v6, 0x40e00000, v6
	v_pk_mul_f32 v[16:17], v[16:17], v[28:29]
	v_min_f32_e32 v7, 0x40e00000, v7
	v_pk_mul_f32 v[16:17], v[14:15], v[16:17]
	s_nop 0
	v_cvt_pk_fp8_f32 v14, v22, v23
	s_nop 0
	v_pk_mul_f32 v[22:23], v[6:7], s[12:13] op_sel_hi:[1,0]
	v_cvt_pk_fp8_f32 v15, v26, v27
	v_exp_f32_e32 v22, v22
	v_exp_f32_e32 v23, v23
	v_pk_fma_f32 v[8:9], v[8:9], v[34:35], v[98:99] op_sel_hi:[1,0,1]
	v_cvt_pk_fp8_f32 v15, v16, v17 op_sel:[0,0,1]
	v_pk_mul_f32 v[16:17], v[110:111], v[18:19]
	v_pk_fma_f32 v[18:19], v[22:23], s[14:15], s[14:15] op_sel_hi:[1,0,0]
	v_pk_fma_f32 v[16:17], v[16:17], v[34:35], v[150:151] op_sel_hi:[1,0,1]
	v_rcp_f32_e32 v18, v18
	v_rcp_f32_e32 v19, v19
	v_med3_f32 v16, v16, s55, v199
	v_med3_f32 v17, v17, s55, v199
	v_min_f32_e32 v8, 0x40e00000, v8
	v_pk_mul_f32 v[6:7], v[6:7], v[18:19]
	v_cvt_f32_i32_e32 v19, v21
	v_cvt_f32_i32_e32 v18, v20
	v_min_f32_e32 v9, 0x40e00000, v9
	v_pk_mul_f32 v[6:7], v[16:17], v[6:7]
	v_pk_fma_f32 v[2:3], v[2:3], v[34:35], v[90:91] op_sel_hi:[1,0,1]
	v_pk_mul_f32 v[16:17], v[112:113], v[18:19]
	v_pk_mul_f32 v[18:19], v[8:9], s[12:13] op_sel_hi:[1,0]
	v_min_f32_e32 v2, 0x40e00000, v2
	v_exp_f32_e32 v18, v18
	v_exp_f32_e32 v19, v19
	v_min_f32_e32 v3, 0x40e00000, v3
	v_pk_mul_f32 v[20:21], v[2:3], s[12:13] op_sel_hi:[1,0]
	v_pk_fma_f32 v[16:17], v[16:17], v[34:35], v[116:117] op_sel_hi:[1,0,1]
	v_pk_fma_f32 v[18:19], v[18:19], s[14:15], s[14:15] op_sel_hi:[1,0,0]
	v_exp_f32_e32 v20, v20
	v_rcp_f32_e32 v18, v18
	v_rcp_f32_e32 v19, v19
	v_exp_f32_e32 v21, v21
	v_med3_f32 v16, v16, s55, v199
	v_med3_f32 v17, v17, s55, v199
	v_pk_mul_f32 v[8:9], v[8:9], v[18:19]
	v_pk_fma_f32 v[10:11], v[10:11], v[34:35], v[100:101] op_sel_hi:[1,0,1]
	v_pk_mul_f32 v[8:9], v[16:17], v[8:9]
	v_pk_fma_f32 v[16:17], v[20:21], s[14:15], s[14:15] op_sel_hi:[1,0,0]
	v_pk_fma_f32 v[4:5], v[4:5], v[34:35], v[74:75] op_sel_hi:[1,0,1]
	v_rcp_f32_e32 v16, v16
	v_rcp_f32_e32 v17, v17
	v_med3_f32 v10, v10, s55, v199
	v_med3_f32 v11, v11, s55, v199
	v_min_f32_e32 v4, 0x40e00000, v4
	v_pk_mul_f32 v[2:3], v[2:3], v[16:17]
	v_min_f32_e32 v5, 0x40e00000, v5
	v_pk_mul_f32 v[2:3], v[10:11], v[2:3]
	v_pk_mul_f32 v[10:11], v[88:89], v[12:13]
	v_pk_mul_f32 v[12:13], v[4:5], s[12:13] op_sel_hi:[1,0]
	s_nop 0
	v_exp_f32_e32 v12, v12
	v_exp_f32_e32 v13, v13
	s_nop 0
	v_cvt_pk_fp8_f32 v16, v6, v7
	v_cvt_pk_fp8_f32 v17, v2, v3
	v_pk_fma_f32 v[12:13], v[12:13], s[14:15], s[14:15] op_sel_hi:[1,0,0]
	v_pk_fma_f32 v[10:11], v[10:11], v[34:35], v[92:93] op_sel_hi:[1,0,1]
	v_rcp_f32_e32 v12, v12
	v_rcp_f32_e32 v13, v13
	v_med3_f32 v10, v10, s55, v199
	v_med3_f32 v11, v11, s55, v199
	v_cvt_pk_fp8_f32 v14, v24, v25 op_sel:[0,0,1]
	v_pk_mul_f32 v[2:3], v[4:5], v[12:13]
	v_cvt_pk_fp8_f32 v16, v8, v9 op_sel:[0,0,1]
	v_pk_mul_f32 v[2:3], v[10:11], v[2:3]
	s_nop 0
	v_permlane16_swap_b32_e32 v14, v16
	v_cvt_pk_fp8_f32 v17, v2, v3 op_sel:[0,0,1]
	v_or_b32_e32 v2, v62, v181
	v_ashrrev_i32_e32 v3, 31, v2
	v_lshlrev_b64 v[2:3], 10, v[2:3]
	v_lshl_add_u64 v[2:3], s[94:95], 0, v[2:3]
	v_permlane16_swap_b32_e32 v15, v17
	v_lshl_add_u64 v[2:3], v[2:3], 0, v[146:147]
	global_store_dwordx4 v[2:3], v[14:17], off
	s_cbranch_vccnz .LBB0_3069
	s_andn2_b64 vcc, exec, s[4:5]
	s_cbranch_vccnz .LBB0_3068
	s_barrier
	s_branch .LBB0_3068

.LBB0_3162:
	s_lshl_b32 s1, s26, 2
	s_add_i32 s1, s1, 0
	s_ashr_i32 s27, s26, 31
	s_add_i32 s1, s1, 0x20480
	s_lshl_b64 s[28:29], s[26:27], 18
	s_add_u32 s28, s78, s28
	s_addc_u32 s29, s79, s29
	s_lshl_b64 s[26:27], s[26:27], 12
	s_add_u32 s30, s49, s26
	v_lshl_or_b32 v20, s24, 8, v206
	s_addc_u32 s31, s50, s27
	v_ashrrev_i32_e32 v21, 31, v20
	s_add_u32 s26, s47, s26
	s_nop 15
	s_nop 15
	v_lshlrev_b64 v[2:3], 2, v[20:21]
	s_addc_u32 s27, s48, s27
	v_lshl_add_u64 v[18:19], s[26:27], 0, v[2:3]
	v_mov_b32_e32 v4, s1
	global_load_dwordx4 v[10:13], v[18:19], off offset:16
	global_load_dwordx4 v[14:17], v[18:19], off
	ds_read_b32 v21, v4
	v_lshl_add_u64 v[22:23], s[30:31], 0, v[2:3]
	global_load_dwordx4 v[6:9], v[22:23], off
	global_load_dwordx4 v[2:5], v[22:23], off offset:16
	v_lshl_add_u32 v219, s22, 8, v1
	v_sub_u32_e32 v32, v20, v175
	s_waitcnt lgkmcnt(0)
	v_sub_u32_e32 v21, s22, v21
	v_lshl_add_u32 v24, v21, 8, v1
	v_ashrrev_i32_e32 v25, 31, v24
	v_lshl_add_u64 v[24:25], v[24:25], 2, s[28:29]
	global_load_dword v26, v[24:25], off
	global_load_dword v27, v[24:25], off offset:64
	global_load_dword v29, v[24:25], off offset:128
	global_load_dword v214, v[24:25], off offset:192
	global_load_dword v215, v[24:25], off offset:512
	global_load_dword v216, v[24:25], off offset:576
	global_load_dword v217, v[24:25], off offset:640
	global_load_dword v218, v[24:25], off offset:704
	v_or_b32_e32 v20, v219, v188
	v_ashrrev_i32_e32 v21, 31, v20
	v_lshlrev_b64 v[20:21], 10, v[20:21]
	v_ashrrev_i32_e32 v33, 31, v32
	v_lshl_add_u64 v[20:21], s[92:93], 0, v[20:21]
	s_nop 0
	v_lshl_add_u64 v[24:25], v[20:21], 0, v[32:33]
	s_nop 0
	s_nop 0
	s_nop 0
	s_andn2_b64 vcc, exec, s[14:15]
	s_mov_b64 s[14:15], -1
	s_waitcnt vmcnt(0)
	v_pk_mul_f32 v[212:213], v[10:11], s[8:9] op_sel_hi:[1,0]
	v_pk_mul_f32 v[184:185], v[16:17], s[8:9] op_sel_hi:[1,0]
	v_pk_mul_f32 v[186:187], v[14:15], s[8:9] op_sel_hi:[1,0]
	v_pk_fma_f32 v[30:31], v[160:161], v[184:185], v[8:9]
	v_pk_fma_f32 v[154:155], v[154:155], v[212:213], v[2:3]
	v_pk_fma_f32 v[160:161], v[146:147], v[212:213], v[2:3]
	v_mul_f32_e32 v146, 4.0, v26
	v_pk_fma_f32 v[158:159], v[158:159], v[186:187], v[6:7]
	v_pk_mul_f32 v[154:155], v[146:147], v[154:155] op_sel_hi:[0,1]
	v_mul_f32_e32 v28, 4.0, v27
	v_pk_mul_f32 v[158:159], v[146:147], v[158:159] op_sel_hi:[0,1]
	v_med3_f32 v21, v154, s57, v209
	v_med3_f32 v27, v155, s57, v209
	v_pk_mul_f32 v[210:211], v[12:13], s[8:9] op_sel_hi:[1,0]
	v_med3_f32 v11, v158, s57, v209
	v_med3_f32 v13, v159, s57, v209
	v_cvt_pk_fp8_f32 v181, v21, v27
	v_pk_fma_f32 v[156:157], v[156:157], v[210:211], v[4:5]
	v_pk_fma_f32 v[150:151], v[150:151], v[186:187], v[6:7]
	v_cvt_pk_fp8_f32 v180, v11, v13
	v_pk_fma_f32 v[152:153], v[152:153], v[184:185], v[8:9]
	v_pk_fma_f32 v[148:149], v[148:149], v[210:211], v[4:5]
	v_mul_f32_e32 v26, 4.0, v29
	v_pk_mul_f32 v[30:31], v[146:147], v[30:31] op_sel_hi:[0,1]
	v_pk_mul_f32 v[156:157], v[146:147], v[156:157] op_sel_hi:[0,1]
	v_pk_mul_f32 v[150:151], v[28:29], v[150:151] op_sel_hi:[0,1]
	v_pk_fma_f32 v[142:143], v[142:143], v[186:187], v[6:7]
	v_pk_mul_f32 v[152:153], v[28:29], v[152:153] op_sel_hi:[0,1]
	v_pk_mul_f32 v[160:161], v[28:29], v[160:161] op_sel_hi:[0,1]
	v_pk_mul_f32 v[148:149], v[28:29], v[148:149] op_sel_hi:[0,1]
	v_med3_f32 v15, v30, s57, v209
	v_med3_f32 v17, v31, s57, v209
	v_med3_f32 v29, v156, s57, v209
	v_med3_f32 v30, v157, s57, v209
	v_med3_f32 v31, v150, s57, v209
	v_med3_f32 v147, v151, s57, v209
	v_pk_mul_f32 v[142:143], v[26:27], v[142:143] op_sel_hi:[0,1]
	v_pk_fma_f32 v[138:139], v[138:139], v[212:213], v[2:3]
	v_cvt_pk_fp8_f32 v182, v31, v147
	v_cvt_pk_fp8_f32 v181, v29, v30 op_sel:[0,0,1]
	v_pk_fma_f32 v[30:31], v[144:145], v[184:185], v[8:9]
	v_pk_mul_f32 v[144:145], v[26:27], v[138:139] op_sel_hi:[0,1]
	v_med3_f32 v11, v142, s57, v209
	v_med3_f32 v13, v143, s57, v209
	s_nop 0
	v_cvt_pk_fp8_f32 v180, v15, v17 op_sel:[0,0,1]
	v_cvt_pk_fp8_f32 v138, v11, v13
	v_med3_f32 v15, v144, s57, v209
	v_med3_f32 v17, v145, s57, v209
	s_nop 0
	v_cvt_pk_fp8_f32 v139, v15, v17
	v_pk_mul_f32 v[30:31], v[26:27], v[30:31] op_sel_hi:[0,1]
	v_pk_fma_f32 v[140:141], v[140:141], v[210:211], v[4:5]
	v_mul_f32_e32 v20, 4.0, v214
	v_pk_mul_f32 v[140:141], v[26:27], v[140:141] op_sel_hi:[0,1]
	v_med3_f32 v11, v30, s57, v209
	v_med3_f32 v13, v31, s57, v209
	v_pk_fma_f32 v[134:135], v[134:135], v[186:187], v[6:7]
	v_cvt_pk_fp8_f32 v138, v11, v13 op_sel:[0,0,1]
	v_med3_f32 v11, v140, s57, v209
	v_med3_f32 v13, v141, s57, v209
	v_pk_mul_f32 v[134:135], v[20:21], v[134:135] op_sel_hi:[0,1]
	v_pk_fma_f32 v[130:131], v[130:131], v[212:213], v[2:3]
	v_cvt_pk_fp8_f32 v139, v11, v13 op_sel:[0,0,1]
	v_pk_mul_f32 v[130:131], v[20:21], v[130:131] op_sel_hi:[0,1]
	v_med3_f32 v11, v134, s57, v209
	v_med3_f32 v13, v135, s57, v209
	s_nop 0
	v_cvt_pk_fp8_f32 v140, v11, v13
	v_med3_f32 v15, v130, s57, v209
	v_med3_f32 v17, v131, s57, v209
	s_nop 0
	v_pk_fma_f32 v[30:31], v[136:137], v[184:185], v[8:9]
	v_cvt_pk_fp8_f32 v141, v15, v17
	v_pk_mul_f32 v[30:31], v[20:21], v[30:31] op_sel_hi:[0,1]
	v_pk_fma_f32 v[132:133], v[132:133], v[210:211], v[4:5]
	v_mul_f32_e32 v16, 4.0, v215
	v_pk_mul_f32 v[132:133], v[20:21], v[132:133] op_sel_hi:[0,1]
	v_med3_f32 v11, v30, s57, v209
	v_med3_f32 v13, v31, s57, v209
	v_pk_fma_f32 v[126:127], v[126:127], v[186:187], v[6:7]
	v_cvt_pk_fp8_f32 v140, v11, v13 op_sel:[0,0,1]
	v_med3_f32 v11, v132, s57, v209
	v_med3_f32 v13, v133, s57, v209
	v_pk_mul_f32 v[126:127], v[16:17], v[126:127] op_sel_hi:[0,1]
	v_pk_fma_f32 v[122:123], v[122:123], v[212:213], v[2:3]
	v_cvt_pk_fp8_f32 v141, v11, v13 op_sel:[0,0,1]
	v_pk_mul_f32 v[130:131], v[16:17], v[122:123] op_sel_hi:[0,1]
	v_med3_f32 v13, v126, s57, v209
	v_med3_f32 v15, v127, s57, v209
	s_nop 0
	v_pk_fma_f32 v[128:129], v[128:129], v[184:185], v[8:9]
	v_pk_fma_f32 v[124:125], v[124:125], v[210:211], v[4:5]
	v_cvt_pk_fp8_f32 v122, v13, v15
	v_pk_mul_f32 v[128:129], v[16:17], v[128:129] op_sel_hi:[0,1]
	v_pk_mul_f32 v[124:125], v[16:17], v[124:125] op_sel_hi:[0,1]
	v_med3_f32 v17, v130, s57, v209
	v_med3_f32 v21, v131, s57, v209
	s_nop 0
	v_cvt_pk_fp8_f32 v123, v17, v21
	v_med3_f32 v13, v128, s57, v209
	v_med3_f32 v15, v129, s57, v209
	v_mul_f32_e32 v14, 4.0, v216
	v_cvt_pk_fp8_f32 v122, v13, v15 op_sel:[0,0,1]
	v_med3_f32 v15, v125, s57, v209
	v_pk_fma_f32 v[118:119], v[118:119], v[186:187], v[6:7]
	v_med3_f32 v13, v124, s57, v209
	v_pk_fma_f32 v[120:121], v[120:121], v[184:185], v[8:9]
	v_pk_mul_f32 v[118:119], v[14:15], v[118:119] op_sel_hi:[0,1]
	v_pk_fma_f32 v[116:117], v[116:117], v[210:211], v[4:5]
	v_pk_fma_f32 v[114:115], v[114:115], v[212:213], v[2:3]
	v_cvt_pk_fp8_f32 v123, v13, v15 op_sel:[0,0,1]
	v_pk_mul_f32 v[120:121], v[14:15], v[120:121] op_sel_hi:[0,1]
	v_pk_mul_f32 v[114:115], v[14:15], v[114:115] op_sel_hi:[0,1]
	v_pk_mul_f32 v[116:117], v[14:15], v[116:117] op_sel_hi:[0,1]
	v_med3_f32 v13, v118, s57, v209
	v_med3_f32 v15, v119, s57, v209
	s_nop 0
	v_cvt_pk_fp8_f32 v124, v13, v15
	v_med3_f32 v17, v114, s57, v209
	v_med3_f32 v21, v115, s57, v209
	s_nop 0
	v_cvt_pk_fp8_f32 v125, v17, v21
	v_med3_f32 v13, v120, s57, v209
	v_med3_f32 v15, v121, s57, v209
	v_mul_f32_e32 v12, 4.0, v217
	v_cvt_pk_fp8_f32 v124, v13, v15 op_sel:[0,0,1]
	v_med3_f32 v13, v116, s57, v209
	v_pk_fma_f32 v[110:111], v[110:111], v[186:187], v[6:7]
	v_med3_f32 v15, v117, s57, v209
	v_pk_fma_f32 v[112:113], v[112:113], v[184:185], v[8:9]
	v_pk_mul_f32 v[110:111], v[12:13], v[110:111] op_sel_hi:[0,1]
	v_pk_fma_f32 v[108:109], v[108:109], v[210:211], v[4:5]
	v_pk_fma_f32 v[106:107], v[106:107], v[212:213], v[2:3]
	v_cvt_pk_fp8_f32 v125, v13, v15 op_sel:[0,0,1]
	v_pk_mul_f32 v[112:113], v[12:13], v[112:113] op_sel_hi:[0,1]
	v_pk_mul_f32 v[116:117], v[12:13], v[106:107] op_sel_hi:[0,1]
	v_pk_mul_f32 v[108:109], v[12:13], v[108:109] op_sel_hi:[0,1]
	v_med3_f32 v13, v110, s57, v209
	v_med3_f32 v15, v111, s57, v209
	s_nop 0
	v_cvt_pk_fp8_f32 v106, v13, v15
	v_mul_f32_e32 v10, 4.0, v218
	v_add_u32_e32 v11, 0x80, v219
	v_pk_fma_f32 v[6:7], v[102:103], v[186:187], v[6:7]
	v_pk_fma_f32 v[2:3], v[94:95], v[212:213], v[2:3]
	v_med3_f32 v13, v112, s57, v209
	v_med3_f32 v15, v113, s57, v209
	v_pk_mul_f32 v[6:7], v[10:11], v[6:7] op_sel_hi:[0,1]
	v_pk_mul_f32 v[2:3], v[10:11], v[2:3] op_sel_hi:[0,1]
	v_med3_f32 v150, v152, s57, v209
	v_med3_f32 v151, v153, s57, v209
	v_med3_f32 v152, v160, s57, v209
	v_med3_f32 v153, v161, s57, v209
	v_med3_f32 v17, v116, s57, v209
	v_med3_f32 v21, v117, s57, v209
	s_nop 0
	v_cvt_pk_fp8_f32 v106, v13, v15 op_sel:[0,0,1]
	v_med3_f32 v13, v108, s57, v209
	v_med3_f32 v15, v109, s57, v209
	v_med3_f32 v6, v6, s57, v209
	v_med3_f32 v7, v7, s57, v209
	s_nop 0
	v_med3_f32 v2, v2, s57, v209
	v_med3_f32 v3, v3, s57, v209
	s_nop 0
	v_cvt_pk_fp8_f32 v183, v152, v153
	v_cvt_pk_fp8_f32 v107, v17, v21
	v_cvt_pk_fp8_f32 v108, v6, v7
	v_cvt_pk_fp8_f32 v109, v2, v3
	v_pk_fma_f32 v[8:9], v[104:105], v[184:185], v[8:9]
	v_pk_fma_f32 v[4:5], v[96:97], v[210:211], v[4:5]
	v_pk_mul_f32 v[8:9], v[10:11], v[8:9] op_sel_hi:[0,1]
	v_pk_mul_f32 v[4:5], v[10:11], v[4:5] op_sel_hi:[0,1]
	v_med3_f32 v148, v148, s57, v209
	v_med3_f32 v149, v149, s57, v209
	v_med3_f32 v6, v8, s57, v209
	v_med3_f32 v7, v9, s57, v209
	v_med3_f32 v2, v4, s57, v209
	v_med3_f32 v3, v5, s57, v209
	v_cvt_pk_fp8_f32 v182, v150, v151 op_sel:[0,0,1]
	v_cvt_pk_fp8_f32 v183, v148, v149 op_sel:[0,0,1]
	v_or_b32_e32 v30, v219, v189
	v_or_b32_e32 v114, v11, v188
	v_cvt_pk_fp8_f32 v107, v13, v15 op_sel:[0,0,1]
	v_cvt_pk_fp8_f32 v108, v6, v7 op_sel:[0,0,1]
	v_cvt_pk_fp8_f32 v109, v2, v3 op_sel:[0,0,1]
	v_or_b32_e32 v2, v11, v189
	v_ashrrev_i32_e32 v31, 31, v30
	v_ashrrev_i32_e32 v115, 31, v114
	v_ashrrev_i32_e32 v3, 31, v2
	v_lshlrev_b64 v[30:31], 10, v[30:31]
	v_lshlrev_b64 v[114:115], 10, v[114:115]
	v_lshlrev_b64 v[2:3], 10, v[2:3]
	v_lshl_add_u64 v[30:31], s[92:93], 0, v[30:31]
	v_lshl_add_u64 v[114:115], s[92:93], 0, v[114:115]
	v_lshl_add_u64 v[2:3], s[92:93], 0, v[2:3]
	v_permlane16_swap_b32_e32 v180, v182
	v_permlane16_swap_b32_e32 v181, v183
	v_permlane16_swap_b32_e32 v138, v140
	v_permlane16_swap_b32_e32 v139, v141
	v_lshl_add_u64 v[30:31], v[30:31], 0, v[32:33]
	v_permlane16_swap_b32_e32 v122, v124
	v_permlane16_swap_b32_e32 v123, v125
	v_lshl_add_u64 v[114:115], v[114:115], 0, v[32:33]
	v_permlane16_swap_b32_e32 v106, v108
	v_permlane16_swap_b32_e32 v107, v109
	v_lshl_add_u64 v[32:33], v[2:3], 0, v[32:33]
	global_store_dwordx4 v[24:25], v[180:183], off
	global_store_dwordx4 v[30:31], v[138:141], off
	global_store_dwordx4 v[114:115], v[122:125], off
	global_store_dwordx4 v[32:33], v[106:109], off
	global_load_dwordx4 v[94:97], v[18:19], off offset:512
	global_load_dwordx4 v[102:105], v[18:19], off offset:528
	global_load_dwordx4 v[6:9], v[22:23], off offset:512
	global_load_dwordx4 v[2:5], v[22:23], off offset:528
	s_waitcnt vmcnt(3)
	v_pk_mul_f32 v[94:95], v[94:95], s[8:9] op_sel_hi:[1,0]
	s_waitcnt vmcnt(2)
	v_pk_mul_f32 v[102:103], v[102:103], s[8:9] op_sel_hi:[1,0]
	s_waitcnt vmcnt(1)
	v_pk_fma_f32 v[98:99], v[98:99], v[94:95], v[6:7]
	v_pk_mul_f32 v[22:23], v[96:97], s[8:9] op_sel_hi:[1,0]
	v_pk_mul_f32 v[98:99], v[146:147], v[98:99] op_sel_hi:[0,1]
	s_waitcnt vmcnt(0)
	v_pk_fma_f32 v[90:91], v[90:91], v[102:103], v[2:3]
	v_pk_fma_f32 v[18:19], v[100:101], v[22:23], v[8:9]
	v_pk_mul_f32 v[100:101], v[146:147], v[90:91] op_sel_hi:[0,1]
	v_med3_f32 v11, v98, s57, v209
	v_med3_f32 v13, v99, s57, v209
	s_nop 0
	v_cvt_pk_fp8_f32 v90, v11, v13
	v_med3_f32 v15, v100, s57, v209
	v_med3_f32 v17, v101, s57, v209
	s_nop 0
	v_pk_mul_f32 v[96:97], v[104:105], s[8:9] op_sel_hi:[1,0]
	v_cvt_pk_fp8_f32 v91, v15, v17
	v_pk_mul_f32 v[18:19], v[146:147], v[18:19] op_sel_hi:[0,1]
	v_pk_fma_f32 v[92:93], v[92:93], v[96:97], v[4:5]
	v_med3_f32 v11, v18, s57, v209
	v_pk_mul_f32 v[92:93], v[146:147], v[92:93] op_sel_hi:[0,1]
	v_med3_f32 v13, v19, s57, v209
	v_pk_fma_f32 v[86:87], v[86:87], v[94:95], v[6:7]
	v_cvt_pk_fp8_f32 v90, v11, v13 op_sel:[0,0,1]
	v_med3_f32 v11, v92, s57, v209
	v_med3_f32 v13, v93, s57, v209
	v_pk_mul_f32 v[86:87], v[28:29], v[86:87] op_sel_hi:[0,1]
	v_pk_fma_f32 v[82:83], v[82:83], v[102:103], v[2:3]
	v_cvt_pk_fp8_f32 v91, v11, v13 op_sel:[0,0,1]
	v_pk_mul_f32 v[82:83], v[28:29], v[82:83] op_sel_hi:[0,1]
	v_med3_f32 v11, v86, s57, v209
	v_med3_f32 v13, v87, s57, v209
	s_nop 0
	v_cvt_pk_fp8_f32 v92, v11, v13
	v_med3_f32 v15, v82, s57, v209
	v_med3_f32 v17, v83, s57, v209
	s_nop 0
	v_pk_fma_f32 v[18:19], v[88:89], v[22:23], v[8:9]
	v_cvt_pk_fp8_f32 v93, v15, v17
	v_pk_mul_f32 v[18:19], v[28:29], v[18:19] op_sel_hi:[0,1]
	v_pk_fma_f32 v[84:85], v[84:85], v[96:97], v[4:5]
	v_med3_f32 v11, v18, s57, v209
	v_pk_mul_f32 v[28:29], v[28:29], v[84:85] op_sel_hi:[0,1]
	v_med3_f32 v13, v19, s57, v209
	v_cvt_pk_fp8_f32 v92, v11, v13 op_sel:[0,0,1]
	v_med3_f32 v11, v28, s57, v209
	v_med3_f32 v13, v29, s57, v209
	v_cvt_pk_fp8_f32 v93, v11, v13 op_sel:[0,0,1]
	v_permlane16_swap_b32_e32 v90, v92
	v_pk_fma_f32 v[18:19], v[80:81], v[22:23], v[8:9]
	v_permlane16_swap_b32_e32 v91, v93
	global_store_dwordx4 v[24:25], v[90:93], off offset:128
	v_pk_fma_f32 v[24:25], v[78:79], v[94:95], v[6:7]
	v_pk_mul_f32 v[28:29], v[26:27], v[18:19] op_sel_hi:[0,1]
	v_pk_mul_f32 v[24:25], v[26:27], v[24:25] op_sel_hi:[0,1]
	v_pk_fma_f32 v[18:19], v[76:77], v[96:97], v[4:5]
	v_pk_fma_f32 v[74:75], v[74:75], v[102:103], v[2:3]
	v_med3_f32 v11, v24, s57, v209
	v_pk_mul_f32 v[74:75], v[26:27], v[74:75] op_sel_hi:[0,1]
	v_pk_mul_f32 v[26:27], v[26:27], v[18:19] op_sel_hi:[0,1]
	v_med3_f32 v13, v25, s57, v209
	s_nop 0
	v_cvt_pk_fp8_f32 v18, v11, v13
	v_med3_f32 v15, v74, s57, v209
	v_med3_f32 v17, v75, s57, v209
	s_nop 0
	v_cvt_pk_fp8_f32 v19, v15, v17
	v_med3_f32 v11, v28, s57, v209
	v_med3_f32 v13, v29, s57, v209
	v_cvt_pk_fp8_f32 v18, v11, v13 op_sel:[0,0,1]
	v_med3_f32 v11, v26, s57, v209
	v_med3_f32 v13, v27, s57, v209
	v_pk_fma_f32 v[26:27], v[62:63], v[94:95], v[6:7]
	v_pk_fma_f32 v[24:25], v[64:65], v[22:23], v[8:9]
	v_pk_mul_f32 v[26:27], v[20:21], v[26:27] op_sel_hi:[0,1]
	v_pk_fma_f32 v[28:29], v[52:53], v[96:97], v[4:5]
	v_pk_fma_f32 v[50:51], v[50:51], v[102:103], v[2:3]
	v_cvt_pk_fp8_f32 v19, v11, v13 op_sel:[0,0,1]
	v_pk_mul_f32 v[24:25], v[20:21], v[24:25] op_sel_hi:[0,1]
	v_pk_mul_f32 v[50:51], v[20:21], v[50:51] op_sel_hi:[0,1]
	v_pk_mul_f32 v[28:29], v[20:21], v[28:29] op_sel_hi:[0,1]
	v_med3_f32 v11, v26, s57, v209
	v_med3_f32 v13, v27, s57, v209
	s_nop 0
	v_cvt_pk_fp8_f32 v20, v11, v13
	v_med3_f32 v15, v50, s57, v209
	v_med3_f32 v17, v51, s57, v209
	s_nop 0
	v_cvt_pk_fp8_f32 v21, v15, v17
	v_med3_f32 v11, v24, s57, v209
	v_med3_f32 v13, v25, s57, v209
	v_cvt_pk_fp8_f32 v20, v11, v13 op_sel:[0,0,1]
	v_med3_f32 v11, v28, s57, v209
	v_med3_f32 v13, v29, s57, v209
	v_cvt_pk_fp8_f32 v21, v11, v13 op_sel:[0,0,1]
	v_permlane16_swap_b32_e32 v18, v20
	v_pk_fma_f32 v[24:25], v[68:69], v[96:97], v[4:5]
	v_permlane16_swap_b32_e32 v19, v21
	global_store_dwordx4 v[30:31], v[18:21], off offset:128
	v_pk_fma_f32 v[26:27], v[66:67], v[102:103], v[2:3]
	v_pk_mul_f32 v[24:25], v[16:17], v[24:25] op_sel_hi:[0,1]
	v_pk_fma_f32 v[20:21], v[70:71], v[94:95], v[6:7]
	v_pk_fma_f32 v[18:19], v[72:73], v[22:23], v[8:9]
	v_pk_mul_f32 v[20:21], v[16:17], v[20:21] op_sel_hi:[0,1]
	v_pk_mul_f32 v[18:19], v[16:17], v[18:19] op_sel_hi:[0,1]
	v_pk_mul_f32 v[26:27], v[16:17], v[26:27] op_sel_hi:[0,1]
	v_med3_f32 v11, v20, s57, v209
	v_med3_f32 v13, v21, s57, v209
	s_nop 0
	v_cvt_pk_fp8_f32 v16, v11, v13
	v_med3_f32 v11, v18, s57, v209
	v_med3_f32 v15, v26, s57, v209
	v_med3_f32 v18, v27, s57, v209
	s_nop 0
	v_cvt_pk_fp8_f32 v17, v15, v18
	v_med3_f32 v13, v19, s57, v209
	v_pk_fma_f32 v[18:19], v[60:61], v[22:23], v[8:9]
	v_pk_fma_f32 v[20:21], v[58:59], v[94:95], v[6:7]
	v_cvt_pk_fp8_f32 v16, v11, v13 op_sel:[0,0,1]
	v_med3_f32 v11, v24, s57, v209
	v_med3_f32 v13, v25, s57, v209
	v_pk_mul_f32 v[20:21], v[14:15], v[20:21] op_sel_hi:[0,1]
	v_pk_mul_f32 v[24:25], v[14:15], v[18:19] op_sel_hi:[0,1]
	v_pk_fma_f32 v[18:19], v[56:57], v[96:97], v[4:5]
	v_pk_fma_f32 v[26:27], v[54:55], v[102:103], v[2:3]
	v_cvt_pk_fp8_f32 v17, v11, v13 op_sel:[0,0,1]
	v_pk_mul_f32 v[26:27], v[14:15], v[26:27] op_sel_hi:[0,1]
	v_pk_mul_f32 v[14:15], v[14:15], v[18:19] op_sel_hi:[0,1]
	v_med3_f32 v11, v20, s57, v209
	v_med3_f32 v13, v21, s57, v209
	s_nop 0
	v_cvt_pk_fp8_f32 v18, v11, v13
	v_med3_f32 v20, v26, s57, v209
	v_med3_f32 v21, v27, s57, v209
	s_nop 0
	v_cvt_pk_fp8_f32 v19, v20, v21
	v_med3_f32 v11, v24, s57, v209
	v_med3_f32 v13, v25, s57, v209
	v_cvt_pk_fp8_f32 v18, v11, v13 op_sel:[0,0,1]
	v_med3_f32 v11, v14, s57, v209
	v_med3_f32 v13, v15, s57, v209
	v_cvt_pk_fp8_f32 v19, v11, v13 op_sel:[0,0,1]
	v_permlane16_swap_b32_e32 v16, v18
	v_pk_fma_f32 v[14:15], v[48:49], v[22:23], v[8:9]
	v_permlane16_swap_b32_e32 v17, v19
	global_store_dwordx4 v[114:115], v[16:19], off offset:128
	v_pk_fma_f32 v[20:21], v[42:43], v[102:103], v[2:3]
	v_pk_mul_f32 v[14:15], v[12:13], v[14:15] op_sel_hi:[0,1]
	v_pk_fma_f32 v[16:17], v[46:47], v[94:95], v[6:7]
	v_pk_fma_f32 v[18:19], v[44:45], v[96:97], v[4:5]
	v_pk_mul_f32 v[16:17], v[12:13], v[16:17] op_sel_hi:[0,1]
	v_pk_mul_f32 v[20:21], v[12:13], v[20:21] op_sel_hi:[0,1]
	v_pk_mul_f32 v[18:19], v[12:13], v[18:19] op_sel_hi:[0,1]
	v_med3_f32 v11, v16, s57, v209
	v_med3_f32 v13, v17, s57, v209
	s_nop 0
	v_cvt_pk_fp8_f32 v12, v11, v13
	v_med3_f32 v11, v14, s57, v209
	v_med3_f32 v14, v15, s57, v209
	v_med3_f32 v15, v20, s57, v209
	v_med3_f32 v16, v21, s57, v209
	s_nop 0
	v_cvt_pk_fp8_f32 v13, v15, v16
	v_cvt_pk_fp8_f32 v12, v11, v14 op_sel:[0,0,1]
	v_med3_f32 v11, v18, s57, v209
	v_pk_fma_f32 v[6:7], v[38:39], v[94:95], v[6:7]
	v_pk_fma_f32 v[2:3], v[34:35], v[102:103], v[2:3]
	v_med3_f32 v14, v19, s57, v209
	v_pk_mul_f32 v[6:7], v[10:11], v[6:7] op_sel_hi:[0,1]
	v_pk_mul_f32 v[2:3], v[10:11], v[2:3] op_sel_hi:[0,1]
	v_cvt_pk_fp8_f32 v13, v11, v14 op_sel:[0,0,1]
	v_med3_f32 v6, v6, s57, v209
	v_med3_f32 v7, v7, s57, v209
	s_nop 0
	v_med3_f32 v2, v2, s57, v209
	v_med3_f32 v3, v3, s57, v209
	s_nop 0
	v_cvt_pk_fp8_f32 v14, v6, v7
	v_cvt_pk_fp8_f32 v15, v2, v3
	v_pk_fma_f32 v[8:9], v[40:41], v[22:23], v[8:9]
	v_pk_fma_f32 v[4:5], v[36:37], v[96:97], v[4:5]
	v_pk_mul_f32 v[8:9], v[10:11], v[8:9] op_sel_hi:[0,1]
	v_pk_mul_f32 v[4:5], v[10:11], v[4:5] op_sel_hi:[0,1]
	v_med3_f32 v6, v8, s57, v209
	v_med3_f32 v7, v9, s57, v209
	v_med3_f32 v2, v4, s57, v209
	v_med3_f32 v3, v5, s57, v209
	v_cvt_pk_fp8_f32 v14, v6, v7 op_sel:[0,0,1]
	v_cvt_pk_fp8_f32 v15, v2, v3 op_sel:[0,0,1]
	s_nop 0
	v_permlane16_swap_b32_e32 v12, v14
	v_permlane16_swap_b32_e32 v13, v15
	global_store_dwordx4 v[32:33], v[12:15], off offset:128
	s_cbranch_vccnz .LBB0_3153
	s_andn2_b64 vcc, exec, s[2:3]
	s_cbranch_vccnz .LBB0_3152
	s_barrier
	s_branch .LBB0_3152
